# GEMM epilogue stores (in-proj, out-proj, PEER query): values and row pointers moved by ds_bpermute so that four neighbouring lanes store 64 contiguous bytes
# baseline (speedup 1.0000x reference)
.LBB0_220:
	v_mbcnt_lo_u32_b32 v243, -1, 0
	v_mbcnt_hi_u32_b32 v243, -1, v243
	v_lshrrev_b32_e32 v244, 2, v243
	v_and_b32_e32 v243, 3, v243
	v_lshl_add_u32 v243, v243, 4, v244
	v_lshlrev_b32_e32 v243, 2, v243
	v_lshl_add_u32 v158, s26, 8, v1
	s_lshl_b32 s19, s0, 8
	v_ashrrev_i32_e32 v159, 31, v158
	v_or_b32_e32 v160, s19, v163
	v_lshl_add_u64 v[156:157], v[158:159], 2, s[66:67]
	global_load_dword v185, v[156:157], off offset:64
	global_load_dword v186, v[156:157], off offset:128
	global_load_dword v187, v[156:157], off offset:192
	global_load_dword v188, v[156:157], off offset:512
	global_load_dword v189, v[156:157], off offset:576
	global_load_dword v190, v[156:157], off offset:640
	global_load_dword v191, v[156:157], off offset:704
	v_ashrrev_i32_e32 v161, 31, v160
	global_load_dword v146, v[156:157], off
	v_lshl_add_u64 v[114:115], v[160:161], 2, s[8:9]
	global_load_dwordx4 v[118:121], v[114:115], off
	s_nop 0
	global_load_dwordx4 v[114:117], v[114:115], off offset:16
	v_cvt_f32_i32_e32 v137, v137
	v_cvt_f32_i32_e32 v136, v136
	v_cvt_f32_i32_e32 v135, v135
	v_cvt_f32_i32_e32 v134, v134
	v_cvt_f32_i32_e32 v133, v133
	v_cvt_f32_i32_e32 v132, v132
	v_cvt_f32_i32_e32 v131, v131
	v_cvt_f32_i32_e32 v130, v130
	s_add_i32 s0, s19, 0xfffff400
	s_cmpk_lt_u32 s0, 0x880
	v_add_u32_e32 v168, 0xffffeb00, v160
	v_cmp_gt_i32_e32 vcc, s65, v160
	s_cselect_b64 s[26:27], -1, 0
	v_cmp_gt_u32_e64 s[0:1], s68, v168
	s_or_b64 vcc, vcc, s[26:27]
	s_waitcnt vmcnt(0)
	v_pk_mul_f32 v[134:135], v[146:147], v[134:135] op_sel_hi:[0,1]
	v_cndmask_b32_e64 v168, 0, v164, s[0:1]
	v_cndmask_b32_e32 v169, v168, v163, vcc
	v_pk_mul_f32 v[136:137], v[146:147], v[136:137] op_sel_hi:[0,1]
	v_pk_mul_f32 v[170:171], v[146:147], v[130:131] op_sel_hi:[0,1]
	v_pk_mul_f32 v[172:173], v[146:147], v[132:133] op_sel_hi:[0,1]
	s_or_b64 s[0:1], s[0:1], vcc
	v_cndmask_b32_e64 v168, 7, 8, vcc
	v_pk_mul_f32 v[132:133], v[120:121], v[136:137]
	v_pk_mul_f32 v[130:131], v[118:119], v[134:135]
	v_pk_mul_f32 v[134:135], v[116:117], v[172:173]
	v_pk_mul_f32 v[136:137], v[114:115], v[170:171]
	v_lshlrev_b32_e32 v146, 1, v169
	s_and_saveexec_b64 s[28:29], s[0:1]
	v_mov_b32_e32 v224, s12
	v_mov_b32_e32 v226, s10
	v_cndmask_b32_e32 v224, v224, v226, vcc
	v_mov_b32_e32 v225, s13
	v_mov_b32_e32 v226, s11
	v_cndmask_b32_e32 v225, v225, v226, vcc
	v_mov_b32_e32 v226, v158
	v_ashrrev_i32_e32 v227, 31, v226
	v_lshlrev_b64 v[228:229], v168, v[226:227]
	v_lshl_add_u64 v[228:229], v[224:225], 0, v[228:229]
	v_lshl_add_u64 v[228:229], v[228:229], 0, v[146:147]
	global_load_dwordx4 v[192:195], v[228:229], off
	v_add_u32_e32 v226, 16, v158
	v_ashrrev_i32_e32 v227, 31, v226
	v_lshlrev_b64 v[228:229], v168, v[226:227]
	v_lshl_add_u64 v[228:229], v[224:225], 0, v[228:229]
	v_lshl_add_u64 v[228:229], v[228:229], 0, v[146:147]
	global_load_dwordx4 v[196:199], v[228:229], off
	v_add_u32_e32 v226, 32, v158
	v_ashrrev_i32_e32 v227, 31, v226
	v_lshlrev_b64 v[228:229], v168, v[226:227]
	v_lshl_add_u64 v[228:229], v[224:225], 0, v[228:229]
	v_lshl_add_u64 v[228:229], v[228:229], 0, v[146:147]
	global_load_dwordx4 v[200:203], v[228:229], off
	v_add_u32_e32 v226, 48, v158
	v_ashrrev_i32_e32 v227, 31, v226
	v_lshlrev_b64 v[228:229], v168, v[226:227]
	v_lshl_add_u64 v[228:229], v[224:225], 0, v[228:229]
	v_lshl_add_u64 v[228:229], v[228:229], 0, v[146:147]
	global_load_dwordx4 v[204:207], v[228:229], off
	v_add_u32_e32 v226, 128, v158
	v_ashrrev_i32_e32 v227, 31, v226
	v_lshlrev_b64 v[228:229], v168, v[226:227]
	v_lshl_add_u64 v[228:229], v[224:225], 0, v[228:229]
	v_lshl_add_u64 v[228:229], v[228:229], 0, v[146:147]
	global_load_dwordx4 v[208:211], v[228:229], off
	v_add_u32_e32 v226, 144, v158
	v_ashrrev_i32_e32 v227, 31, v226
	v_lshlrev_b64 v[228:229], v168, v[226:227]
	v_lshl_add_u64 v[228:229], v[224:225], 0, v[228:229]
	v_lshl_add_u64 v[228:229], v[228:229], 0, v[146:147]
	global_load_dwordx4 v[212:215], v[228:229], off
	v_add_u32_e32 v226, 160, v158
	v_ashrrev_i32_e32 v227, 31, v226
	v_lshlrev_b64 v[228:229], v168, v[226:227]
	v_lshl_add_u64 v[228:229], v[224:225], 0, v[228:229]
	v_lshl_add_u64 v[228:229], v[228:229], 0, v[146:147]
	global_load_dwordx4 v[216:219], v[228:229], off
	v_add_u32_e32 v226, 176, v158
	v_ashrrev_i32_e32 v227, 31, v226
	v_lshlrev_b64 v[228:229], v168, v[226:227]
	v_lshl_add_u64 v[228:229], v[224:225], 0, v[228:229]
	v_lshl_add_u64 v[228:229], v[228:229], 0, v[146:147]
	global_load_dwordx4 v[220:223], v[228:229], off
	s_or_b64 exec, exec, s[28:29]
	s_waitcnt vmcnt(0)
	s_and_saveexec_b64 s[26:27], s[0:1]
	s_cbranch_execz .LBB0_222
	v_mov_b32_e32 v169, s13
	v_mov_b32_e32 v170, s11
	v_cndmask_b32_e32 v171, v169, v170, vcc
	v_mov_b32_e32 v169, s12
	v_mov_b32_e32 v170, s10
	v_cndmask_b32_e32 v170, v169, v170, vcc
	v_lshlrev_b64 v[172:173], v168, v[158:159]
	v_lshl_add_u64 v[170:171], v[170:171], 0, v[172:173]
	v_lshl_add_u64 v[170:171], v[170:171], 0, v[146:147]
	v_mov_b64_e32 v[170:171], v[192:193]
	v_mov_b64_e32 v[172:173], v[194:195]
	v_cvt_f32_f16_e32 v178, v172
	v_cvt_f32_f16_sdwa v179, v172 dst_sel:DWORD dst_unused:UNUSED_PAD src0_sel:WORD_1
	v_cvt_f32_f16_e32 v172, v173
	v_cvt_f32_f16_sdwa v173, v173 dst_sel:DWORD dst_unused:UNUSED_PAD src0_sel:WORD_1
	v_cvt_f32_f16_e32 v176, v170
	v_cvt_f32_f16_sdwa v177, v170 dst_sel:DWORD dst_unused:UNUSED_PAD src0_sel:WORD_1
	v_cvt_f32_f16_e32 v170, v171
	v_cvt_f32_f16_sdwa v171, v171 dst_sel:DWORD dst_unused:UNUSED_PAD src0_sel:WORD_1
	v_pk_mul_f32 v[180:181], v[136:137], v[178:179]
	v_pk_mul_f32 v[182:183], v[134:135], v[172:173]
	v_pk_mul_f32 v[178:179], v[130:131], v[178:179]
	v_pk_mul_f32 v[172:173], v[132:133], v[172:173]
	v_pk_fma_f32 v[132:133], v[132:133], v[170:171], v[182:183] neg_lo:[0,0,1] neg_hi:[0,0,1]
	v_pk_fma_f32 v[130:131], v[130:131], v[176:177], v[180:181] neg_lo:[0,0,1] neg_hi:[0,0,1]
	v_pk_fma_f32 v[134:135], v[134:135], v[170:171], v[172:173]
	v_pk_fma_f32 v[136:137], v[136:137], v[176:177], v[178:179]
.LBB0_222:
	s_or_b64 exec, exec, s[26:27]
	v_cvt_pk_bf16_f32 v170, v130, v131
	v_mov_b64_e32 v[130:131], s[82:83]
	v_mad_i64_i32 v[130:131], s[26:27], v158, s69, v[130:131]
	v_cvt_pk_bf16_f32 v171, v132, v133
	v_lshl_add_u64 v[132:133], v[160:161], 1, v[130:131]
	v_or_b32_e32 v130, 16, v158
	v_ashrrev_i32_e32 v131, 31, v130
	v_cvt_pk_bf16_f32 v172, v136, v137
	v_cvt_pk_bf16_f32 v173, v134, v135
	ds_bpermute_b32 v240, v243, v132
	ds_bpermute_b32 v241, v243, v133
	ds_bpermute_b32 v244, v243, v170
	ds_bpermute_b32 v245, v243, v171
	ds_bpermute_b32 v246, v243, v172
	ds_bpermute_b32 v247, v243, v173
	s_waitcnt lgkmcnt(0)
	global_store_dwordx4 v[240:241], v[244:247], off
	v_lshl_add_u64 v[134:135], v[130:131], 2, s[66:67]
	s_nop 1
	v_mov_b32_e32 v136, v185
	v_cvt_f32_i32_e32 v129, v129
	v_cvt_f32_i32_e32 v128, v128
	v_cvt_f32_i32_e32 v127, v127
	v_cvt_f32_i32_e32 v126, v126
	v_cvt_f32_i32_e32 v125, v125
	v_cvt_f32_i32_e32 v123, v123
	v_cvt_f32_i32_e32 v122, v122
	v_cvt_f32_i32_e32 v124, v124
	v_pk_mul_f32 v[126:127], v[136:137], v[126:127] op_sel_hi:[0,1]
	v_pk_mul_f32 v[128:129], v[136:137], v[128:129] op_sel_hi:[0,1]
	v_pk_mul_f32 v[170:171], v[136:137], v[122:123] op_sel_hi:[0,1]
	v_pk_mul_f32 v[136:137], v[136:137], v[124:125] op_sel_hi:[0,1]
	v_pk_mul_f32 v[124:125], v[120:121], v[128:129]
	v_pk_mul_f32 v[122:123], v[118:119], v[126:127]
	v_pk_mul_f32 v[126:127], v[116:117], v[136:137]
	v_pk_mul_f32 v[128:129], v[114:115], v[170:171]
	s_and_saveexec_b64 s[26:27], s[0:1]
	s_cbranch_execz .LBB0_224
	v_mov_b32_e32 v136, s13
	v_mov_b32_e32 v137, s11
	v_cndmask_b32_e32 v137, v136, v137, vcc
	v_mov_b32_e32 v136, s12
	v_mov_b32_e32 v169, s10
	v_cndmask_b32_e32 v136, v136, v169, vcc
	v_lshlrev_b64 v[170:171], v168, v[130:131]
	v_lshl_add_u64 v[136:137], v[136:137], 0, v[170:171]
	v_lshl_add_u64 v[136:137], v[136:137], 0, v[146:147]
	v_mov_b64_e32 v[170:171], v[196:197]
	v_mov_b64_e32 v[172:173], v[198:199]
	v_cvt_f32_f16_e32 v176, v172
	v_cvt_f32_f16_sdwa v177, v172 dst_sel:DWORD dst_unused:UNUSED_PAD src0_sel:WORD_1
	v_cvt_f32_f16_e32 v172, v173
	v_cvt_f32_f16_sdwa v173, v173 dst_sel:DWORD dst_unused:UNUSED_PAD src0_sel:WORD_1
	v_cvt_f32_f16_e32 v136, v170
	v_cvt_f32_f16_sdwa v137, v170 dst_sel:DWORD dst_unused:UNUSED_PAD src0_sel:WORD_1
	v_cvt_f32_f16_e32 v170, v171
	v_cvt_f32_f16_sdwa v171, v171 dst_sel:DWORD dst_unused:UNUSED_PAD src0_sel:WORD_1
	v_pk_mul_f32 v[178:179], v[128:129], v[176:177]
	v_pk_mul_f32 v[180:181], v[126:127], v[172:173]
	v_pk_mul_f32 v[176:177], v[122:123], v[176:177]
	v_pk_mul_f32 v[172:173], v[124:125], v[172:173]
	v_pk_fma_f32 v[124:125], v[124:125], v[170:171], v[180:181] neg_lo:[0,0,1] neg_hi:[0,0,1]
	v_pk_fma_f32 v[122:123], v[122:123], v[136:137], v[178:179] neg_lo:[0,0,1] neg_hi:[0,0,1]
	v_pk_fma_f32 v[126:127], v[126:127], v[170:171], v[172:173]
	v_pk_fma_f32 v[128:129], v[128:129], v[136:137], v[176:177]
.LBB0_224:
	s_or_b64 exec, exec, s[26:27]
	v_cvt_pk_bf16_f32 v170, v122, v123
	v_mov_b64_e32 v[122:123], s[82:83]
	v_mad_i64_i32 v[122:123], s[26:27], v130, s69, v[122:123]
	v_cvt_pk_bf16_f32 v171, v124, v125
	v_lshl_add_u64 v[124:125], v[160:161], 1, v[122:123]
	v_or_b32_e32 v122, 32, v158
	v_ashrrev_i32_e32 v123, 31, v122
	v_cvt_pk_bf16_f32 v172, v128, v129
	v_cvt_pk_bf16_f32 v173, v126, v127
	ds_bpermute_b32 v240, v243, v124
	ds_bpermute_b32 v241, v243, v125
	ds_bpermute_b32 v244, v243, v170
	ds_bpermute_b32 v245, v243, v171
	ds_bpermute_b32 v246, v243, v172
	ds_bpermute_b32 v247, v243, v173
	s_waitcnt lgkmcnt(0)
	global_store_dwordx4 v[240:241], v[244:247], off
	v_lshl_add_u64 v[126:127], v[122:123], 2, s[66:67]
	s_nop 1
	v_mov_b32_e32 v128, v186
	v_cvt_f32_i32_e32 v113, v113
	v_cvt_f32_i32_e32 v112, v112
	v_cvt_f32_i32_e32 v111, v111
	v_cvt_f32_i32_e32 v110, v110
	v_cvt_f32_i32_e32 v109, v109
	v_cvt_f32_i32_e32 v107, v107
	v_cvt_f32_i32_e32 v106, v106
	v_cvt_f32_i32_e32 v108, v108
	v_pk_mul_f32 v[110:111], v[128:129], v[110:111] op_sel_hi:[0,1]
	v_pk_mul_f32 v[112:113], v[128:129], v[112:113] op_sel_hi:[0,1]
	v_pk_mul_f32 v[136:137], v[128:129], v[106:107] op_sel_hi:[0,1]
	v_pk_mul_f32 v[128:129], v[128:129], v[108:109] op_sel_hi:[0,1]
	v_pk_mul_f32 v[108:109], v[120:121], v[112:113]
	v_pk_mul_f32 v[106:107], v[118:119], v[110:111]
	v_pk_mul_f32 v[110:111], v[116:117], v[128:129]
	v_pk_mul_f32 v[112:113], v[114:115], v[136:137]
	s_and_saveexec_b64 s[26:27], s[0:1]
	v_readlane_b32 s74, v242, 37
	v_readlane_b32 s75, v242, 38
	s_cbranch_execz .LBB0_226
	v_mov_b32_e32 v128, s13
	v_mov_b32_e32 v129, s11
	v_cndmask_b32_e32 v129, v128, v129, vcc
	v_mov_b32_e32 v128, s12
	v_mov_b32_e32 v136, s10
	v_cndmask_b32_e32 v128, v128, v136, vcc
	v_lshlrev_b64 v[136:137], v168, v[122:123]
	v_lshl_add_u64 v[128:129], v[128:129], 0, v[136:137]
	v_lshl_add_u64 v[128:129], v[128:129], 0, v[146:147]
	v_mov_b64_e32 v[170:171], v[200:201]
	v_mov_b64_e32 v[172:173], v[202:203]
	v_cvt_f32_f16_e32 v136, v172
	v_cvt_f32_f16_sdwa v137, v172 dst_sel:DWORD dst_unused:UNUSED_PAD src0_sel:WORD_1
	v_cvt_f32_f16_e32 v172, v173
	v_cvt_f32_f16_sdwa v173, v173 dst_sel:DWORD dst_unused:UNUSED_PAD src0_sel:WORD_1
	v_cvt_f32_f16_e32 v128, v170
	v_cvt_f32_f16_sdwa v129, v170 dst_sel:DWORD dst_unused:UNUSED_PAD src0_sel:WORD_1
	v_cvt_f32_f16_e32 v170, v171
	v_cvt_f32_f16_sdwa v171, v171 dst_sel:DWORD dst_unused:UNUSED_PAD src0_sel:WORD_1
	v_pk_mul_f32 v[176:177], v[112:113], v[136:137]
	v_pk_mul_f32 v[178:179], v[110:111], v[172:173]
	v_pk_mul_f32 v[136:137], v[106:107], v[136:137]
	v_pk_mul_f32 v[172:173], v[108:109], v[172:173]
	v_pk_fma_f32 v[108:109], v[108:109], v[170:171], v[178:179] neg_lo:[0,0,1] neg_hi:[0,0,1]
	v_pk_fma_f32 v[106:107], v[106:107], v[128:129], v[176:177] neg_lo:[0,0,1] neg_hi:[0,0,1]
	v_pk_fma_f32 v[110:111], v[110:111], v[170:171], v[172:173]
	v_pk_fma_f32 v[112:113], v[112:113], v[128:129], v[136:137]
.LBB0_226:
	s_or_b64 exec, exec, s[26:27]
	v_cvt_pk_bf16_f32 v170, v106, v107
	v_mov_b64_e32 v[106:107], s[82:83]
	v_mad_i64_i32 v[106:107], s[26:27], v122, s69, v[106:107]
	v_cvt_pk_bf16_f32 v171, v108, v109
	v_lshl_add_u64 v[108:109], v[160:161], 1, v[106:107]
	v_or_b32_e32 v106, 48, v158
	v_ashrrev_i32_e32 v107, 31, v106
	v_cvt_pk_bf16_f32 v172, v112, v113
	v_cvt_pk_bf16_f32 v173, v110, v111
	ds_bpermute_b32 v240, v243, v108
	ds_bpermute_b32 v241, v243, v109
	ds_bpermute_b32 v244, v243, v170
	ds_bpermute_b32 v245, v243, v171
	ds_bpermute_b32 v246, v243, v172
	ds_bpermute_b32 v247, v243, v173
	s_waitcnt lgkmcnt(0)
	global_store_dwordx4 v[240:241], v[244:247], off
	v_lshl_add_u64 v[110:111], v[106:107], 2, s[66:67]
	s_nop 1
	v_mov_b32_e32 v112, v187
	v_cvt_f32_i32_e32 v105, v105
	v_cvt_f32_i32_e32 v104, v104
	v_cvt_f32_i32_e32 v103, v103
	v_cvt_f32_i32_e32 v102, v102
	v_cvt_f32_i32_e32 v101, v101
	v_cvt_f32_i32_e32 v99, v99
	v_cvt_f32_i32_e32 v98, v98
	v_cvt_f32_i32_e32 v100, v100
	v_pk_mul_f32 v[102:103], v[112:113], v[102:103] op_sel_hi:[0,1]
	v_pk_mul_f32 v[104:105], v[112:113], v[104:105] op_sel_hi:[0,1]
	v_pk_mul_f32 v[128:129], v[112:113], v[98:99] op_sel_hi:[0,1]
	v_pk_mul_f32 v[112:113], v[112:113], v[100:101] op_sel_hi:[0,1]
	v_pk_mul_f32 v[100:101], v[120:121], v[104:105]
	v_pk_mul_f32 v[98:99], v[118:119], v[102:103]
	v_pk_mul_f32 v[102:103], v[116:117], v[112:113]
	v_pk_mul_f32 v[104:105], v[114:115], v[128:129]
	s_and_saveexec_b64 s[26:27], s[0:1]
	s_cbranch_execz .LBB0_228
	v_mov_b32_e32 v112, s13
	v_mov_b32_e32 v113, s11
	v_cndmask_b32_e32 v113, v112, v113, vcc
	v_mov_b32_e32 v112, s12
	v_mov_b32_e32 v128, s10
	v_cndmask_b32_e32 v112, v112, v128, vcc
	v_lshlrev_b64 v[128:129], v168, v[106:107]
	v_lshl_add_u64 v[112:113], v[112:113], 0, v[128:129]
	v_lshl_add_u64 v[112:113], v[112:113], 0, v[146:147]
	v_mov_b64_e32 v[170:171], v[204:205]
	v_mov_b64_e32 v[172:173], v[206:207]
	v_cvt_f32_f16_e32 v128, v172
	v_cvt_f32_f16_sdwa v129, v172 dst_sel:DWORD dst_unused:UNUSED_PAD src0_sel:WORD_1
	v_cvt_f32_f16_e32 v136, v173
	v_cvt_f32_f16_sdwa v137, v173 dst_sel:DWORD dst_unused:UNUSED_PAD src0_sel:WORD_1
	v_cvt_f32_f16_e32 v112, v170
	v_cvt_f32_f16_sdwa v113, v170 dst_sel:DWORD dst_unused:UNUSED_PAD src0_sel:WORD_1
	v_cvt_f32_f16_e32 v170, v171
	v_cvt_f32_f16_sdwa v171, v171 dst_sel:DWORD dst_unused:UNUSED_PAD src0_sel:WORD_1
	v_pk_mul_f32 v[172:173], v[104:105], v[128:129]
	v_pk_mul_f32 v[176:177], v[102:103], v[136:137]
	v_pk_mul_f32 v[128:129], v[98:99], v[128:129]
	v_pk_mul_f32 v[136:137], v[100:101], v[136:137]
	v_pk_fma_f32 v[100:101], v[100:101], v[170:171], v[176:177] neg_lo:[0,0,1] neg_hi:[0,0,1]
	v_pk_fma_f32 v[98:99], v[98:99], v[112:113], v[172:173] neg_lo:[0,0,1] neg_hi:[0,0,1]
	v_pk_fma_f32 v[102:103], v[102:103], v[170:171], v[136:137]
	v_pk_fma_f32 v[104:105], v[104:105], v[112:113], v[128:129]
.LBB0_228:
	s_or_b64 exec, exec, s[26:27]
	v_cvt_pk_bf16_f32 v170, v98, v99
	v_mov_b64_e32 v[98:99], s[82:83]
	v_mad_i64_i32 v[98:99], s[26:27], v106, s69, v[98:99]
	v_cvt_pk_bf16_f32 v171, v100, v101
	v_lshl_add_u64 v[100:101], v[160:161], 1, v[98:99]
	v_cvt_pk_bf16_f32 v172, v104, v105
	v_cvt_pk_bf16_f32 v173, v102, v103
	ds_bpermute_b32 v240, v243, v100
	ds_bpermute_b32 v241, v243, v101
	ds_bpermute_b32 v244, v243, v170
	ds_bpermute_b32 v245, v243, v171
	ds_bpermute_b32 v246, v243, v172
	ds_bpermute_b32 v247, v243, v173
	s_waitcnt lgkmcnt(0)
	global_store_dwordx4 v[240:241], v[244:247], off
	s_nop 1
	v_mov_b32_e32 v102, v188
	v_cvt_f32_i32_e32 v97, v97
	v_cvt_f32_i32_e32 v96, v96
	v_cvt_f32_i32_e32 v95, v95
	v_cvt_f32_i32_e32 v94, v94
	v_cvt_f32_i32_e32 v93, v93
	v_cvt_f32_i32_e32 v92, v92
	v_cvt_f32_i32_e32 v91, v91
	v_cvt_f32_i32_e32 v90, v90
	v_add_u32_e32 v98, 0x80, v158
	v_ashrrev_i32_e32 v99, 31, v98
	v_pk_mul_f32 v[94:95], v[102:103], v[94:95] op_sel_hi:[0,1]
	v_pk_mul_f32 v[96:97], v[102:103], v[96:97] op_sel_hi:[0,1]
	v_pk_mul_f32 v[104:105], v[102:103], v[90:91] op_sel_hi:[0,1]
	v_pk_mul_f32 v[102:103], v[102:103], v[92:93] op_sel_hi:[0,1]
	v_pk_mul_f32 v[92:93], v[120:121], v[96:97]
	v_pk_mul_f32 v[90:91], v[118:119], v[94:95]
	v_pk_mul_f32 v[94:95], v[116:117], v[102:103]
	v_pk_mul_f32 v[96:97], v[114:115], v[104:105]
	s_and_saveexec_b64 s[26:27], s[0:1]
	s_cbranch_execz .LBB0_230
	v_mov_b32_e32 v102, s13
	v_mov_b32_e32 v103, s11
	v_cndmask_b32_e32 v103, v102, v103, vcc
	v_mov_b32_e32 v102, s12
	v_mov_b32_e32 v104, s10
	v_cndmask_b32_e32 v102, v102, v104, vcc
	v_lshlrev_b64 v[104:105], v168, v[98:99]
	v_lshl_add_u64 v[102:103], v[102:103], 0, v[104:105]
	v_lshl_add_u64 v[102:103], v[102:103], 0, v[146:147]
	v_mov_b64_e32 v[102:103], v[208:209]
	v_mov_b64_e32 v[104:105], v[210:211]
	v_cvt_f32_f16_e32 v128, v104
	v_cvt_f32_f16_sdwa v129, v104 dst_sel:DWORD dst_unused:UNUSED_PAD src0_sel:WORD_1
	v_cvt_f32_f16_e32 v104, v105
	v_cvt_f32_f16_sdwa v105, v105 dst_sel:DWORD dst_unused:UNUSED_PAD src0_sel:WORD_1
	v_cvt_f32_f16_e32 v112, v102
	v_cvt_f32_f16_sdwa v113, v102 dst_sel:DWORD dst_unused:UNUSED_PAD src0_sel:WORD_1
	v_cvt_f32_f16_e32 v102, v103
	v_cvt_f32_f16_sdwa v103, v103 dst_sel:DWORD dst_unused:UNUSED_PAD src0_sel:WORD_1
	v_pk_mul_f32 v[136:137], v[96:97], v[128:129]
	v_pk_mul_f32 v[170:171], v[94:95], v[104:105]
	v_pk_mul_f32 v[128:129], v[90:91], v[128:129]
	v_pk_mul_f32 v[104:105], v[92:93], v[104:105]
	v_pk_fma_f32 v[92:93], v[92:93], v[102:103], v[170:171] neg_lo:[0,0,1] neg_hi:[0,0,1]
	v_pk_fma_f32 v[90:91], v[90:91], v[112:113], v[136:137] neg_lo:[0,0,1] neg_hi:[0,0,1]
	v_pk_fma_f32 v[94:95], v[94:95], v[102:103], v[104:105]
	v_pk_fma_f32 v[96:97], v[96:97], v[112:113], v[128:129]
.LBB0_230:
	s_or_b64 exec, exec, s[26:27]
	v_cvt_pk_bf16_f32 v102, v90, v91
	v_mov_b64_e32 v[90:91], s[82:83]
	v_mad_i64_i32 v[90:91], s[26:27], v98, s69, v[90:91]
	v_cvt_pk_bf16_f32 v103, v92, v93
	v_lshl_add_u64 v[92:93], v[160:161], 1, v[90:91]
	v_cvt_pk_bf16_f32 v104, v96, v97
	v_cvt_pk_bf16_f32 v105, v94, v95
	ds_bpermute_b32 v240, v243, v92
	ds_bpermute_b32 v241, v243, v93
	ds_bpermute_b32 v244, v243, v102
	ds_bpermute_b32 v245, v243, v103
	ds_bpermute_b32 v246, v243, v104
	ds_bpermute_b32 v247, v243, v105
	s_waitcnt lgkmcnt(0)
	global_store_dwordx4 v[240:241], v[244:247], off
	s_nop 1
	v_mov_b32_e32 v94, v189
	v_cvt_f32_i32_e32 v89, v89
	v_cvt_f32_i32_e32 v88, v88
	v_cvt_f32_i32_e32 v87, v87
	v_cvt_f32_i32_e32 v86, v86
	v_cvt_f32_i32_e32 v85, v85
	v_cvt_f32_i32_e32 v84, v84
	v_cvt_f32_i32_e32 v83, v83
	v_cvt_f32_i32_e32 v82, v82
	v_add_u32_e32 v90, 0x90, v158
	v_ashrrev_i32_e32 v91, 31, v90
	v_pk_mul_f32 v[86:87], v[94:95], v[86:87] op_sel_hi:[0,1]
	v_pk_mul_f32 v[88:89], v[94:95], v[88:89] op_sel_hi:[0,1]
	v_pk_mul_f32 v[96:97], v[94:95], v[82:83] op_sel_hi:[0,1]
	v_pk_mul_f32 v[94:95], v[94:95], v[84:85] op_sel_hi:[0,1]
	v_pk_mul_f32 v[84:85], v[120:121], v[88:89]
	v_pk_mul_f32 v[82:83], v[118:119], v[86:87]
	v_pk_mul_f32 v[86:87], v[116:117], v[94:95]
	v_pk_mul_f32 v[88:89], v[114:115], v[96:97]
	s_and_saveexec_b64 s[26:27], s[0:1]
	s_cbranch_execz .LBB0_232
	v_mov_b32_e32 v94, s13
	v_mov_b32_e32 v95, s11
	v_cndmask_b32_e32 v95, v94, v95, vcc
	v_mov_b32_e32 v94, s12
	v_mov_b32_e32 v96, s10
	v_cndmask_b32_e32 v94, v94, v96, vcc
	v_lshlrev_b64 v[96:97], v168, v[90:91]
	v_lshl_add_u64 v[94:95], v[94:95], 0, v[96:97]
	v_lshl_add_u64 v[94:95], v[94:95], 0, v[146:147]
	v_mov_b64_e32 v[94:95], v[212:213]
	v_mov_b64_e32 v[96:97], v[214:215]
	v_cvt_f32_f16_e32 v104, v96
	v_cvt_f32_f16_sdwa v105, v96 dst_sel:DWORD dst_unused:UNUSED_PAD src0_sel:WORD_1
	v_cvt_f32_f16_e32 v96, v97
	v_cvt_f32_f16_sdwa v97, v97 dst_sel:DWORD dst_unused:UNUSED_PAD src0_sel:WORD_1
	v_cvt_f32_f16_e32 v102, v94
	v_cvt_f32_f16_sdwa v103, v94 dst_sel:DWORD dst_unused:UNUSED_PAD src0_sel:WORD_1
	v_cvt_f32_f16_e32 v94, v95
	v_cvt_f32_f16_sdwa v95, v95 dst_sel:DWORD dst_unused:UNUSED_PAD src0_sel:WORD_1
	v_pk_mul_f32 v[112:113], v[88:89], v[104:105]
	v_pk_mul_f32 v[128:129], v[86:87], v[96:97]
	v_pk_mul_f32 v[104:105], v[82:83], v[104:105]
	v_pk_mul_f32 v[96:97], v[84:85], v[96:97]
	v_pk_fma_f32 v[84:85], v[84:85], v[94:95], v[128:129] neg_lo:[0,0,1] neg_hi:[0,0,1]
	v_pk_fma_f32 v[82:83], v[82:83], v[102:103], v[112:113] neg_lo:[0,0,1] neg_hi:[0,0,1]
	v_pk_fma_f32 v[86:87], v[86:87], v[94:95], v[96:97]
	v_pk_fma_f32 v[88:89], v[88:89], v[102:103], v[104:105]
.LBB0_232:
	s_or_b64 exec, exec, s[26:27]
	v_cvt_pk_bf16_f32 v94, v82, v83
	v_mov_b64_e32 v[82:83], s[82:83]
	v_mad_i64_i32 v[82:83], s[26:27], v90, s69, v[82:83]
	v_cvt_pk_bf16_f32 v95, v84, v85
	v_lshl_add_u64 v[84:85], v[160:161], 1, v[82:83]
	v_cvt_pk_bf16_f32 v96, v88, v89
	v_cvt_pk_bf16_f32 v97, v86, v87
	ds_bpermute_b32 v240, v243, v84
	ds_bpermute_b32 v241, v243, v85
	ds_bpermute_b32 v244, v243, v94
	ds_bpermute_b32 v245, v243, v95
	ds_bpermute_b32 v246, v243, v96
	ds_bpermute_b32 v247, v243, v97
	s_waitcnt lgkmcnt(0)
	global_store_dwordx4 v[240:241], v[244:247], off
	s_nop 1
	v_mov_b32_e32 v86, v190
	v_cvt_f32_i32_e32 v81, v81
	v_cvt_f32_i32_e32 v80, v80
	v_cvt_f32_i32_e32 v79, v79
	v_cvt_f32_i32_e32 v78, v78
	v_cvt_f32_i32_e32 v77, v77
	v_cvt_f32_i32_e32 v76, v76
	v_cvt_f32_i32_e32 v75, v75
	v_cvt_f32_i32_e32 v74, v74
	v_add_u32_e32 v82, 0xa0, v158
	v_ashrrev_i32_e32 v83, 31, v82
	v_pk_mul_f32 v[78:79], v[86:87], v[78:79] op_sel_hi:[0,1]
	v_pk_mul_f32 v[80:81], v[86:87], v[80:81] op_sel_hi:[0,1]
	v_pk_mul_f32 v[88:89], v[86:87], v[74:75] op_sel_hi:[0,1]
	v_pk_mul_f32 v[86:87], v[86:87], v[76:77] op_sel_hi:[0,1]
	v_pk_mul_f32 v[76:77], v[120:121], v[80:81]
	v_pk_mul_f32 v[74:75], v[118:119], v[78:79]
	v_pk_mul_f32 v[78:79], v[116:117], v[86:87]
	v_pk_mul_f32 v[80:81], v[114:115], v[88:89]
	s_and_saveexec_b64 s[26:27], s[0:1]
	s_cbranch_execz .LBB0_234
	v_mov_b32_e32 v86, s13
	v_mov_b32_e32 v87, s11
	v_cndmask_b32_e32 v87, v86, v87, vcc
	v_mov_b32_e32 v86, s12
	v_mov_b32_e32 v88, s10
	v_cndmask_b32_e32 v86, v86, v88, vcc
	v_lshlrev_b64 v[88:89], v168, v[82:83]
	v_lshl_add_u64 v[86:87], v[86:87], 0, v[88:89]
	v_lshl_add_u64 v[86:87], v[86:87], 0, v[146:147]
	v_mov_b64_e32 v[86:87], v[216:217]
	v_mov_b64_e32 v[88:89], v[218:219]
	v_cvt_f32_f16_e32 v96, v88
	v_cvt_f32_f16_sdwa v97, v88 dst_sel:DWORD dst_unused:UNUSED_PAD src0_sel:WORD_1
	v_cvt_f32_f16_e32 v88, v89
	v_cvt_f32_f16_sdwa v89, v89 dst_sel:DWORD dst_unused:UNUSED_PAD src0_sel:WORD_1
	v_cvt_f32_f16_e32 v94, v86
	v_cvt_f32_f16_sdwa v95, v86 dst_sel:DWORD dst_unused:UNUSED_PAD src0_sel:WORD_1
	v_cvt_f32_f16_e32 v86, v87
	v_cvt_f32_f16_sdwa v87, v87 dst_sel:DWORD dst_unused:UNUSED_PAD src0_sel:WORD_1
	v_pk_mul_f32 v[102:103], v[80:81], v[96:97]
	v_pk_mul_f32 v[104:105], v[78:79], v[88:89]
	v_pk_mul_f32 v[96:97], v[74:75], v[96:97]
	v_pk_mul_f32 v[88:89], v[76:77], v[88:89]
	v_pk_fma_f32 v[76:77], v[76:77], v[86:87], v[104:105] neg_lo:[0,0,1] neg_hi:[0,0,1]
	v_pk_fma_f32 v[74:75], v[74:75], v[94:95], v[102:103] neg_lo:[0,0,1] neg_hi:[0,0,1]
	v_pk_fma_f32 v[78:79], v[78:79], v[86:87], v[88:89]
	v_pk_fma_f32 v[80:81], v[80:81], v[94:95], v[96:97]
.LBB0_234:
	s_or_b64 exec, exec, s[26:27]
	v_cvt_pk_bf16_f32 v86, v74, v75
	v_mov_b64_e32 v[74:75], s[82:83]
	v_mad_i64_i32 v[74:75], s[26:27], v82, s69, v[74:75]
	v_cvt_pk_bf16_f32 v87, v76, v77
	v_lshl_add_u64 v[76:77], v[160:161], 1, v[74:75]
	v_cvt_pk_bf16_f32 v88, v80, v81
	v_cvt_pk_bf16_f32 v89, v78, v79
	ds_bpermute_b32 v240, v243, v76
	ds_bpermute_b32 v241, v243, v77
	ds_bpermute_b32 v244, v243, v86
	ds_bpermute_b32 v245, v243, v87
	ds_bpermute_b32 v246, v243, v88
	ds_bpermute_b32 v247, v243, v89
	s_waitcnt lgkmcnt(0)
	global_store_dwordx4 v[240:241], v[244:247], off
	s_nop 1
	v_mov_b32_e32 v78, v191
	v_cvt_f32_i32_e32 v73, v73
	v_cvt_f32_i32_e32 v72, v72
	v_cvt_f32_i32_e32 v71, v71
	v_cvt_f32_i32_e32 v70, v70
	v_cvt_f32_i32_e32 v69, v69
	v_cvt_f32_i32_e32 v68, v68
	v_cvt_f32_i32_e32 v67, v67
	v_cvt_f32_i32_e32 v66, v66
	v_add_u32_e32 v74, 0xb0, v158
	v_ashrrev_i32_e32 v75, 31, v74
	v_pk_mul_f32 v[70:71], v[78:79], v[70:71] op_sel_hi:[0,1]
	v_pk_mul_f32 v[72:73], v[78:79], v[72:73] op_sel_hi:[0,1]
	v_pk_mul_f32 v[80:81], v[78:79], v[66:67] op_sel_hi:[0,1]
	v_pk_mul_f32 v[78:79], v[78:79], v[68:69] op_sel_hi:[0,1]
	v_pk_mul_f32 v[68:69], v[120:121], v[72:73]
	v_pk_mul_f32 v[66:67], v[118:119], v[70:71]
	v_pk_mul_f32 v[70:71], v[116:117], v[78:79]
	v_pk_mul_f32 v[72:73], v[114:115], v[80:81]
	s_and_saveexec_b64 s[26:27], s[0:1]
	s_cbranch_execz .LBB0_236
	v_mov_b32_e32 v78, s13
	v_mov_b32_e32 v79, s11
	v_cndmask_b32_e32 v79, v78, v79, vcc
	v_mov_b32_e32 v78, s12
	v_mov_b32_e32 v80, s10
	v_cndmask_b32_e32 v78, v78, v80, vcc
	v_lshlrev_b64 v[80:81], v168, v[74:75]
	v_lshl_add_u64 v[78:79], v[78:79], 0, v[80:81]
	v_lshl_add_u64 v[78:79], v[78:79], 0, v[146:147]
	v_mov_b64_e32 v[78:79], v[220:221]
	v_mov_b64_e32 v[80:81], v[222:223]
	v_cvt_f32_f16_e32 v88, v80
	v_cvt_f32_f16_sdwa v89, v80 dst_sel:DWORD dst_unused:UNUSED_PAD src0_sel:WORD_1
	v_cvt_f32_f16_e32 v80, v81
	v_cvt_f32_f16_sdwa v81, v81 dst_sel:DWORD dst_unused:UNUSED_PAD src0_sel:WORD_1
	v_cvt_f32_f16_e32 v86, v78
	v_cvt_f32_f16_sdwa v87, v78 dst_sel:DWORD dst_unused:UNUSED_PAD src0_sel:WORD_1
	v_cvt_f32_f16_e32 v78, v79
	v_cvt_f32_f16_sdwa v79, v79 dst_sel:DWORD dst_unused:UNUSED_PAD src0_sel:WORD_1
	v_pk_mul_f32 v[94:95], v[72:73], v[88:89]
	v_pk_mul_f32 v[96:97], v[70:71], v[80:81]
	v_pk_mul_f32 v[88:89], v[66:67], v[88:89]
	v_pk_mul_f32 v[80:81], v[68:69], v[80:81]
	v_pk_fma_f32 v[68:69], v[68:69], v[78:79], v[96:97] neg_lo:[0,0,1] neg_hi:[0,0,1]
	v_pk_fma_f32 v[66:67], v[66:67], v[86:87], v[94:95] neg_lo:[0,0,1] neg_hi:[0,0,1]
	v_pk_fma_f32 v[70:71], v[70:71], v[78:79], v[80:81]
	v_pk_fma_f32 v[72:73], v[72:73], v[86:87], v[88:89]
.LBB0_236:
	s_or_b64 exec, exec, s[26:27]
	v_cvt_pk_bf16_f32 v66, v66, v67
	v_cvt_pk_bf16_f32 v67, v68, v69
	v_cvt_pk_bf16_f32 v68, v72, v73
	v_cvt_pk_bf16_f32 v69, v70, v71
	v_mov_b64_e32 v[70:71], s[82:83]
	v_mad_i64_i32 v[70:71], s[0:1], v74, s69, v[70:71]
	v_lshl_add_u64 v[78:79], v[160:161], 1, v[70:71]
	v_or_b32_e32 v80, 0x80, v160
	ds_bpermute_b32 v240, v243, v78
	ds_bpermute_b32 v241, v243, v79
	ds_bpermute_b32 v244, v243, v66
	ds_bpermute_b32 v245, v243, v67
	ds_bpermute_b32 v246, v243, v68
	ds_bpermute_b32 v247, v243, v69
	s_waitcnt lgkmcnt(0)
	global_store_dwordx4 v[240:241], v[244:247], off
	v_ashrrev_i32_e32 v81, 31, v80
	global_load_dword v86, v[156:157], off
	v_lshl_add_u64 v[66:67], v[80:81], 2, s[8:9]
	global_load_dwordx4 v[70:73], v[66:67], off
	s_nop 0
	global_load_dwordx4 v[66:69], v[66:67], off offset:16
	s_addk_i32 s19, 0xf480
	v_cvt_f32_i32_e32 v65, v65
	v_cvt_f32_i32_e32 v64, v64
	v_cvt_f32_i32_e32 v63, v63
	v_cvt_f32_i32_e32 v62, v62
	v_cvt_f32_i32_e32 v61, v61
	v_cvt_f32_i32_e32 v60, v60
	v_cvt_f32_i32_e32 v59, v59
	v_cvt_f32_i32_e32 v58, v58
	v_add_u32_e32 v81, 0xffffeb80, v160
	s_cmpk_lt_u32 s19, 0x880
	v_cmp_gt_i32_e32 vcc, s65, v80
	v_cmp_gt_u32_e64 s[0:1], s68, v81
	s_cselect_b64 s[26:27], -1, 0
	s_or_b64 vcc, vcc, s[26:27]
	v_cndmask_b32_e64 v80, 0, v164, s[0:1]
	v_cndmask_b32_e32 v81, v80, v163, vcc
	s_or_b64 s[0:1], s[0:1], vcc
	v_cndmask_b32_e64 v80, 7, 8, vcc
	v_lshlrev_b32_e32 v146, 1, v81
	s_waitcnt vmcnt(2)
	v_pk_mul_f32 v[62:63], v[86:87], v[62:63] op_sel_hi:[0,1]
	v_pk_mul_f32 v[64:65], v[86:87], v[64:65] op_sel_hi:[0,1]
	v_pk_mul_f32 v[88:89], v[86:87], v[58:59] op_sel_hi:[0,1]
	v_pk_mul_f32 v[86:87], v[86:87], v[60:61] op_sel_hi:[0,1]
	s_waitcnt vmcnt(1)
	v_pk_mul_f32 v[60:61], v[72:73], v[64:65]
	v_pk_mul_f32 v[58:59], v[70:71], v[62:63]
	s_waitcnt vmcnt(0)
	v_pk_mul_f32 v[62:63], v[68:69], v[86:87]
	v_pk_mul_f32 v[64:65], v[66:67], v[88:89]
	s_and_saveexec_b64 s[28:29], s[0:1]
	v_mov_b32_e32 v224, s12
	v_mov_b32_e32 v226, s10
	v_cndmask_b32_e32 v224, v224, v226, vcc
	v_mov_b32_e32 v225, s13
	v_mov_b32_e32 v226, s11
	v_cndmask_b32_e32 v225, v225, v226, vcc
	v_mov_b32_e32 v226, v158
	v_ashrrev_i32_e32 v227, 31, v226
	v_lshlrev_b64 v[228:229], v80, v[226:227]
	v_lshl_add_u64 v[228:229], v[224:225], 0, v[228:229]
	v_lshl_add_u64 v[228:229], v[228:229], 0, v[146:147]
	global_load_dwordx4 v[192:195], v[228:229], off
	v_add_u32_e32 v226, 16, v158
	v_ashrrev_i32_e32 v227, 31, v226
	v_lshlrev_b64 v[228:229], v80, v[226:227]
	v_lshl_add_u64 v[228:229], v[224:225], 0, v[228:229]
	v_lshl_add_u64 v[228:229], v[228:229], 0, v[146:147]
	global_load_dwordx4 v[196:199], v[228:229], off
	v_add_u32_e32 v226, 32, v158
	v_ashrrev_i32_e32 v227, 31, v226
	v_lshlrev_b64 v[228:229], v80, v[226:227]
	v_lshl_add_u64 v[228:229], v[224:225], 0, v[228:229]
	v_lshl_add_u64 v[228:229], v[228:229], 0, v[146:147]
	global_load_dwordx4 v[200:203], v[228:229], off
	v_add_u32_e32 v226, 48, v158
	v_ashrrev_i32_e32 v227, 31, v226
	v_lshlrev_b64 v[228:229], v80, v[226:227]
	v_lshl_add_u64 v[228:229], v[224:225], 0, v[228:229]
	v_lshl_add_u64 v[228:229], v[228:229], 0, v[146:147]
	global_load_dwordx4 v[204:207], v[228:229], off
	v_add_u32_e32 v226, 128, v158
	v_ashrrev_i32_e32 v227, 31, v226
	v_lshlrev_b64 v[228:229], v80, v[226:227]
	v_lshl_add_u64 v[228:229], v[224:225], 0, v[228:229]
	v_lshl_add_u64 v[228:229], v[228:229], 0, v[146:147]
	global_load_dwordx4 v[208:211], v[228:229], off
	v_add_u32_e32 v226, 144, v158
	v_ashrrev_i32_e32 v227, 31, v226
	v_lshlrev_b64 v[228:229], v80, v[226:227]
	v_lshl_add_u64 v[228:229], v[224:225], 0, v[228:229]
	v_lshl_add_u64 v[228:229], v[228:229], 0, v[146:147]
	global_load_dwordx4 v[212:215], v[228:229], off
	v_add_u32_e32 v226, 160, v158
	v_ashrrev_i32_e32 v227, 31, v226
	v_lshlrev_b64 v[228:229], v80, v[226:227]
	v_lshl_add_u64 v[228:229], v[224:225], 0, v[228:229]
	v_lshl_add_u64 v[228:229], v[228:229], 0, v[146:147]
	global_load_dwordx4 v[216:219], v[228:229], off
	v_add_u32_e32 v226, 176, v158
	v_ashrrev_i32_e32 v227, 31, v226
	v_lshlrev_b64 v[228:229], v80, v[226:227]
	v_lshl_add_u64 v[228:229], v[224:225], 0, v[228:229]
	v_lshl_add_u64 v[228:229], v[228:229], 0, v[146:147]
	global_load_dwordx4 v[220:223], v[228:229], off
	s_or_b64 exec, exec, s[28:29]
	s_waitcnt vmcnt(0)
	s_and_saveexec_b64 s[26:27], s[0:1]
	s_cbranch_execz .LBB0_238
	v_mov_b32_e32 v81, s13
	v_mov_b32_e32 v86, s11
	v_cndmask_b32_e32 v87, v81, v86, vcc
	v_mov_b32_e32 v81, s12
	v_mov_b32_e32 v86, s10
	v_cndmask_b32_e32 v86, v81, v86, vcc
	v_lshlrev_b64 v[88:89], v80, v[158:159]
	v_lshl_add_u64 v[86:87], v[86:87], 0, v[88:89]
	v_lshl_add_u64 v[86:87], v[86:87], 0, v[146:147]
	v_mov_b64_e32 v[86:87], v[192:193]
	v_mov_b64_e32 v[88:89], v[194:195]
	v_cvt_f32_f16_e32 v96, v88
	v_cvt_f32_f16_sdwa v97, v88 dst_sel:DWORD dst_unused:UNUSED_PAD src0_sel:WORD_1
	v_cvt_f32_f16_e32 v88, v89
	v_cvt_f32_f16_sdwa v89, v89 dst_sel:DWORD dst_unused:UNUSED_PAD src0_sel:WORD_1
	v_cvt_f32_f16_e32 v94, v86
	v_cvt_f32_f16_sdwa v95, v86 dst_sel:DWORD dst_unused:UNUSED_PAD src0_sel:WORD_1
	v_cvt_f32_f16_e32 v86, v87
	v_cvt_f32_f16_sdwa v87, v87 dst_sel:DWORD dst_unused:UNUSED_PAD src0_sel:WORD_1
	v_pk_mul_f32 v[102:103], v[64:65], v[96:97]
	v_pk_mul_f32 v[104:105], v[62:63], v[88:89]
	v_pk_mul_f32 v[96:97], v[58:59], v[96:97]
	v_pk_mul_f32 v[88:89], v[60:61], v[88:89]
	v_pk_fma_f32 v[60:61], v[60:61], v[86:87], v[104:105] neg_lo:[0,0,1] neg_hi:[0,0,1]
	v_pk_fma_f32 v[58:59], v[58:59], v[94:95], v[102:103] neg_lo:[0,0,1] neg_hi:[0,0,1]
	v_pk_fma_f32 v[62:63], v[62:63], v[86:87], v[88:89]
	v_pk_fma_f32 v[64:65], v[64:65], v[94:95], v[96:97]
.LBB0_238:
	s_or_b64 exec, exec, s[26:27]
	v_cvt_pk_bf16_f32 v58, v58, v59
	v_cvt_pk_bf16_f32 v59, v60, v61
	v_cvt_pk_bf16_f32 v60, v64, v65
	v_cvt_pk_bf16_f32 v61, v62, v63
	ds_bpermute_b32 v240, v243, v132
	ds_bpermute_b32 v241, v243, v133
	ds_bpermute_b32 v244, v243, v58
	ds_bpermute_b32 v245, v243, v59
	ds_bpermute_b32 v246, v243, v60
	ds_bpermute_b32 v247, v243, v61
	s_waitcnt lgkmcnt(0)
	global_store_dwordx4 v[240:241], v[244:247], off offset:256
	s_nop 1
	v_mov_b32_e32 v58, v185
	v_cvt_f32_i32_e32 v57, v57
	v_cvt_f32_i32_e32 v56, v56
	v_cvt_f32_i32_e32 v55, v55
	v_cvt_f32_i32_e32 v54, v54
	v_cvt_f32_i32_e32 v53, v53
	v_cvt_f32_i32_e32 v51, v51
	v_cvt_f32_i32_e32 v50, v50
	v_cvt_f32_i32_e32 v52, v52
	v_pk_mul_f32 v[54:55], v[58:59], v[54:55] op_sel_hi:[0,1]
	v_pk_mul_f32 v[56:57], v[58:59], v[56:57] op_sel_hi:[0,1]
	v_pk_mul_f32 v[60:61], v[58:59], v[50:51] op_sel_hi:[0,1]
	v_pk_mul_f32 v[58:59], v[58:59], v[52:53] op_sel_hi:[0,1]
	v_pk_mul_f32 v[52:53], v[72:73], v[56:57]
	v_pk_mul_f32 v[50:51], v[70:71], v[54:55]
	v_pk_mul_f32 v[54:55], v[68:69], v[58:59]
	v_pk_mul_f32 v[56:57], v[66:67], v[60:61]
	s_and_saveexec_b64 s[26:27], s[0:1]
	s_cbranch_execz .LBB0_240
	v_mov_b32_e32 v58, s13
	v_mov_b32_e32 v59, s11
	v_cndmask_b32_e32 v59, v58, v59, vcc
	v_mov_b32_e32 v58, s12
	v_mov_b32_e32 v60, s10
	v_cndmask_b32_e32 v58, v58, v60, vcc
	v_lshlrev_b64 v[60:61], v80, v[130:131]
	v_lshl_add_u64 v[58:59], v[58:59], 0, v[60:61]
	v_lshl_add_u64 v[58:59], v[58:59], 0, v[146:147]
	v_mov_b64_e32 v[58:59], v[196:197]
	v_mov_b64_e32 v[60:61], v[198:199]
	v_cvt_f32_f16_e32 v64, v60
	v_cvt_f32_f16_sdwa v65, v60 dst_sel:DWORD dst_unused:UNUSED_PAD src0_sel:WORD_1
	v_cvt_f32_f16_e32 v60, v61
	v_cvt_f32_f16_sdwa v61, v61 dst_sel:DWORD dst_unused:UNUSED_PAD src0_sel:WORD_1
	v_cvt_f32_f16_e32 v62, v58
	v_cvt_f32_f16_sdwa v63, v58 dst_sel:DWORD dst_unused:UNUSED_PAD src0_sel:WORD_1
	v_cvt_f32_f16_e32 v58, v59
	v_cvt_f32_f16_sdwa v59, v59 dst_sel:DWORD dst_unused:UNUSED_PAD src0_sel:WORD_1
	v_pk_mul_f32 v[86:87], v[56:57], v[64:65]
	v_pk_mul_f32 v[88:89], v[54:55], v[60:61]
	v_pk_mul_f32 v[64:65], v[50:51], v[64:65]
	v_pk_mul_f32 v[60:61], v[52:53], v[60:61]
	v_pk_fma_f32 v[52:53], v[52:53], v[58:59], v[88:89] neg_lo:[0,0,1] neg_hi:[0,0,1]
	v_pk_fma_f32 v[50:51], v[50:51], v[62:63], v[86:87] neg_lo:[0,0,1] neg_hi:[0,0,1]
	v_pk_fma_f32 v[54:55], v[54:55], v[58:59], v[60:61]
	v_pk_fma_f32 v[56:57], v[56:57], v[62:63], v[64:65]
.LBB0_240:
	s_or_b64 exec, exec, s[26:27]
	v_cvt_pk_bf16_f32 v50, v50, v51
	v_cvt_pk_bf16_f32 v51, v52, v53
	v_cvt_pk_bf16_f32 v52, v56, v57
	v_cvt_pk_bf16_f32 v53, v54, v55
	ds_bpermute_b32 v240, v243, v124
	ds_bpermute_b32 v241, v243, v125
	ds_bpermute_b32 v244, v243, v50
	ds_bpermute_b32 v245, v243, v51
	ds_bpermute_b32 v246, v243, v52
	ds_bpermute_b32 v247, v243, v53
	s_waitcnt lgkmcnt(0)
	global_store_dwordx4 v[240:241], v[244:247], off offset:256
	s_nop 1
	v_mov_b32_e32 v50, v186
	v_cvt_f32_i32_e32 v49, v49
	v_cvt_f32_i32_e32 v48, v48
	v_cvt_f32_i32_e32 v47, v47
	v_cvt_f32_i32_e32 v46, v46
	v_cvt_f32_i32_e32 v45, v45
	v_cvt_f32_i32_e32 v43, v43
	v_cvt_f32_i32_e32 v42, v42
	v_cvt_f32_i32_e32 v44, v44
	v_pk_mul_f32 v[46:47], v[50:51], v[46:47] op_sel_hi:[0,1]
	v_pk_mul_f32 v[48:49], v[50:51], v[48:49] op_sel_hi:[0,1]
	v_pk_mul_f32 v[52:53], v[50:51], v[42:43] op_sel_hi:[0,1]
	v_pk_mul_f32 v[50:51], v[50:51], v[44:45] op_sel_hi:[0,1]
	v_pk_mul_f32 v[44:45], v[72:73], v[48:49]
	v_pk_mul_f32 v[42:43], v[70:71], v[46:47]
	v_pk_mul_f32 v[46:47], v[68:69], v[50:51]
	v_pk_mul_f32 v[48:49], v[66:67], v[52:53]
	s_and_saveexec_b64 s[26:27], s[0:1]
	s_cbranch_execz .LBB0_242
	v_mov_b32_e32 v50, s13
	v_mov_b32_e32 v51, s11
	v_cndmask_b32_e32 v51, v50, v51, vcc
	v_mov_b32_e32 v50, s12
	v_mov_b32_e32 v52, s10
	v_cndmask_b32_e32 v50, v50, v52, vcc
	v_lshlrev_b64 v[52:53], v80, v[122:123]
	v_lshl_add_u64 v[50:51], v[50:51], 0, v[52:53]
	v_lshl_add_u64 v[50:51], v[50:51], 0, v[146:147]
	v_mov_b64_e32 v[50:51], v[200:201]
	v_mov_b64_e32 v[52:53], v[202:203]
	v_cvt_f32_f16_e32 v56, v52
	v_cvt_f32_f16_sdwa v57, v52 dst_sel:DWORD dst_unused:UNUSED_PAD src0_sel:WORD_1
	v_cvt_f32_f16_e32 v52, v53
	v_cvt_f32_f16_sdwa v53, v53 dst_sel:DWORD dst_unused:UNUSED_PAD src0_sel:WORD_1
	v_cvt_f32_f16_e32 v54, v50
	v_cvt_f32_f16_sdwa v55, v50 dst_sel:DWORD dst_unused:UNUSED_PAD src0_sel:WORD_1
	v_cvt_f32_f16_e32 v50, v51
	v_cvt_f32_f16_sdwa v51, v51 dst_sel:DWORD dst_unused:UNUSED_PAD src0_sel:WORD_1
	v_pk_mul_f32 v[58:59], v[48:49], v[56:57]
	v_pk_mul_f32 v[60:61], v[46:47], v[52:53]
	v_pk_mul_f32 v[56:57], v[42:43], v[56:57]
	v_pk_mul_f32 v[52:53], v[44:45], v[52:53]
	v_pk_fma_f32 v[44:45], v[44:45], v[50:51], v[60:61] neg_lo:[0,0,1] neg_hi:[0,0,1]
	v_pk_fma_f32 v[42:43], v[42:43], v[54:55], v[58:59] neg_lo:[0,0,1] neg_hi:[0,0,1]
	v_pk_fma_f32 v[46:47], v[46:47], v[50:51], v[52:53]
	v_pk_fma_f32 v[48:49], v[48:49], v[54:55], v[56:57]
.LBB0_242:
	s_or_b64 exec, exec, s[26:27]
	v_cvt_pk_bf16_f32 v42, v42, v43
	v_cvt_pk_bf16_f32 v43, v44, v45
	v_cvt_pk_bf16_f32 v44, v48, v49
	v_cvt_pk_bf16_f32 v45, v46, v47
	ds_bpermute_b32 v240, v243, v108
	ds_bpermute_b32 v241, v243, v109
	ds_bpermute_b32 v244, v243, v42
	ds_bpermute_b32 v245, v243, v43
	ds_bpermute_b32 v246, v243, v44
	ds_bpermute_b32 v247, v243, v45
	s_waitcnt lgkmcnt(0)
	global_store_dwordx4 v[240:241], v[244:247], off offset:256
	s_nop 1
	v_mov_b32_e32 v42, v187
	v_cvt_f32_i32_e32 v41, v41
	v_cvt_f32_i32_e32 v40, v40
	v_cvt_f32_i32_e32 v39, v39
	v_cvt_f32_i32_e32 v38, v38
	v_cvt_f32_i32_e32 v37, v37
	v_cvt_f32_i32_e32 v35, v35
	v_cvt_f32_i32_e32 v34, v34
	v_cvt_f32_i32_e32 v36, v36
	v_pk_mul_f32 v[38:39], v[42:43], v[38:39] op_sel_hi:[0,1]
	v_pk_mul_f32 v[40:41], v[42:43], v[40:41] op_sel_hi:[0,1]
	v_pk_mul_f32 v[44:45], v[42:43], v[34:35] op_sel_hi:[0,1]
	v_pk_mul_f32 v[42:43], v[42:43], v[36:37] op_sel_hi:[0,1]
	v_pk_mul_f32 v[36:37], v[72:73], v[40:41]
	v_pk_mul_f32 v[34:35], v[70:71], v[38:39]
	v_pk_mul_f32 v[38:39], v[68:69], v[42:43]
	v_pk_mul_f32 v[40:41], v[66:67], v[44:45]
	s_and_saveexec_b64 s[26:27], s[0:1]
	s_cbranch_execz .LBB0_244
	v_mov_b32_e32 v42, s13
	v_mov_b32_e32 v43, s11
	v_cndmask_b32_e32 v43, v42, v43, vcc
	v_mov_b32_e32 v42, s12
	v_mov_b32_e32 v44, s10
	v_cndmask_b32_e32 v42, v42, v44, vcc
	v_lshlrev_b64 v[44:45], v80, v[106:107]
	v_lshl_add_u64 v[42:43], v[42:43], 0, v[44:45]
	v_lshl_add_u64 v[42:43], v[42:43], 0, v[146:147]
	v_mov_b64_e32 v[42:43], v[204:205]
	v_mov_b64_e32 v[44:45], v[206:207]
	v_cvt_f32_f16_e32 v48, v44
	v_cvt_f32_f16_sdwa v49, v44 dst_sel:DWORD dst_unused:UNUSED_PAD src0_sel:WORD_1
	v_cvt_f32_f16_e32 v44, v45
	v_cvt_f32_f16_sdwa v45, v45 dst_sel:DWORD dst_unused:UNUSED_PAD src0_sel:WORD_1
	v_cvt_f32_f16_e32 v46, v42
	v_cvt_f32_f16_sdwa v47, v42 dst_sel:DWORD dst_unused:UNUSED_PAD src0_sel:WORD_1
	v_cvt_f32_f16_e32 v42, v43
	v_cvt_f32_f16_sdwa v43, v43 dst_sel:DWORD dst_unused:UNUSED_PAD src0_sel:WORD_1
	v_pk_mul_f32 v[50:51], v[40:41], v[48:49]
	v_pk_mul_f32 v[52:53], v[38:39], v[44:45]
	v_pk_mul_f32 v[48:49], v[34:35], v[48:49]
	v_pk_mul_f32 v[44:45], v[36:37], v[44:45]
	v_pk_fma_f32 v[36:37], v[36:37], v[42:43], v[52:53] neg_lo:[0,0,1] neg_hi:[0,0,1]
	v_pk_fma_f32 v[34:35], v[34:35], v[46:47], v[50:51] neg_lo:[0,0,1] neg_hi:[0,0,1]
	v_pk_fma_f32 v[38:39], v[38:39], v[42:43], v[44:45]
	v_pk_fma_f32 v[40:41], v[40:41], v[46:47], v[48:49]
.LBB0_244:
	s_or_b64 exec, exec, s[26:27]
	v_cvt_pk_bf16_f32 v34, v34, v35
	v_cvt_pk_bf16_f32 v35, v36, v37
	v_cvt_pk_bf16_f32 v36, v40, v41
	v_cvt_pk_bf16_f32 v37, v38, v39
	ds_bpermute_b32 v240, v243, v100
	ds_bpermute_b32 v241, v243, v101
	ds_bpermute_b32 v244, v243, v34
	ds_bpermute_b32 v245, v243, v35
	ds_bpermute_b32 v246, v243, v36
	ds_bpermute_b32 v247, v243, v37
	s_waitcnt lgkmcnt(0)
	global_store_dwordx4 v[240:241], v[244:247], off offset:256
	s_nop 1
	v_mov_b32_e32 v34, v188
	v_cvt_f32_i32_e32 v33, v33
	v_cvt_f32_i32_e32 v32, v32
	v_cvt_f32_i32_e32 v31, v31
	v_cvt_f32_i32_e32 v30, v30
	v_cvt_f32_i32_e32 v29, v29
	v_cvt_f32_i32_e32 v27, v27
	v_cvt_f32_i32_e32 v26, v26
	v_cvt_f32_i32_e32 v28, v28
	v_pk_mul_f32 v[30:31], v[34:35], v[30:31] op_sel_hi:[0,1]
	v_pk_mul_f32 v[32:33], v[34:35], v[32:33] op_sel_hi:[0,1]
	v_pk_mul_f32 v[36:37], v[34:35], v[26:27] op_sel_hi:[0,1]
	v_pk_mul_f32 v[34:35], v[34:35], v[28:29] op_sel_hi:[0,1]
	v_pk_mul_f32 v[28:29], v[72:73], v[32:33]
	v_pk_mul_f32 v[26:27], v[70:71], v[30:31]
	v_pk_mul_f32 v[30:31], v[68:69], v[34:35]
	v_pk_mul_f32 v[32:33], v[66:67], v[36:37]
	s_and_saveexec_b64 s[26:27], s[0:1]
	s_cbranch_execz .LBB0_246
	v_mov_b32_e32 v34, s13
	v_mov_b32_e32 v35, s11
	v_cndmask_b32_e32 v35, v34, v35, vcc
	v_mov_b32_e32 v34, s12
	v_mov_b32_e32 v36, s10
	v_cndmask_b32_e32 v34, v34, v36, vcc
	v_lshlrev_b64 v[36:37], v80, v[98:99]
	v_lshl_add_u64 v[34:35], v[34:35], 0, v[36:37]
	v_lshl_add_u64 v[34:35], v[34:35], 0, v[146:147]
	v_mov_b64_e32 v[34:35], v[208:209]
	v_mov_b64_e32 v[36:37], v[210:211]
	v_cvt_f32_f16_e32 v40, v36
	v_cvt_f32_f16_sdwa v41, v36 dst_sel:DWORD dst_unused:UNUSED_PAD src0_sel:WORD_1
	v_cvt_f32_f16_e32 v36, v37
	v_cvt_f32_f16_sdwa v37, v37 dst_sel:DWORD dst_unused:UNUSED_PAD src0_sel:WORD_1
	v_cvt_f32_f16_e32 v38, v34
	v_cvt_f32_f16_sdwa v39, v34 dst_sel:DWORD dst_unused:UNUSED_PAD src0_sel:WORD_1
	v_cvt_f32_f16_e32 v34, v35
	v_cvt_f32_f16_sdwa v35, v35 dst_sel:DWORD dst_unused:UNUSED_PAD src0_sel:WORD_1
	v_pk_mul_f32 v[42:43], v[32:33], v[40:41]
	v_pk_mul_f32 v[44:45], v[30:31], v[36:37]
	v_pk_mul_f32 v[40:41], v[26:27], v[40:41]
	v_pk_mul_f32 v[36:37], v[28:29], v[36:37]
	v_pk_fma_f32 v[28:29], v[28:29], v[34:35], v[44:45] neg_lo:[0,0,1] neg_hi:[0,0,1]
	v_pk_fma_f32 v[26:27], v[26:27], v[38:39], v[42:43] neg_lo:[0,0,1] neg_hi:[0,0,1]
	v_pk_fma_f32 v[30:31], v[30:31], v[34:35], v[36:37]
	v_pk_fma_f32 v[32:33], v[32:33], v[38:39], v[40:41]
.LBB0_246:
	s_or_b64 exec, exec, s[26:27]
	v_cvt_pk_bf16_f32 v26, v26, v27
	v_cvt_pk_bf16_f32 v27, v28, v29
	v_cvt_pk_bf16_f32 v28, v32, v33
	v_cvt_pk_bf16_f32 v29, v30, v31
	ds_bpermute_b32 v240, v243, v92
	ds_bpermute_b32 v241, v243, v93
	ds_bpermute_b32 v244, v243, v26
	ds_bpermute_b32 v245, v243, v27
	ds_bpermute_b32 v246, v243, v28
	ds_bpermute_b32 v247, v243, v29
	s_waitcnt lgkmcnt(0)
	global_store_dwordx4 v[240:241], v[244:247], off offset:256
	s_nop 1
	v_mov_b32_e32 v26, v189
	v_cvt_f32_i32_e32 v25, v25
	v_cvt_f32_i32_e32 v24, v24
	v_cvt_f32_i32_e32 v23, v23
	v_cvt_f32_i32_e32 v22, v22
	v_cvt_f32_i32_e32 v21, v21
	v_cvt_f32_i32_e32 v19, v19
	v_cvt_f32_i32_e32 v18, v18
	v_cvt_f32_i32_e32 v20, v20
	v_pk_mul_f32 v[22:23], v[26:27], v[22:23] op_sel_hi:[0,1]
	v_pk_mul_f32 v[24:25], v[26:27], v[24:25] op_sel_hi:[0,1]
	v_pk_mul_f32 v[28:29], v[26:27], v[18:19] op_sel_hi:[0,1]
	v_pk_mul_f32 v[26:27], v[26:27], v[20:21] op_sel_hi:[0,1]
	v_pk_mul_f32 v[20:21], v[72:73], v[24:25]
	v_pk_mul_f32 v[18:19], v[70:71], v[22:23]
	v_pk_mul_f32 v[22:23], v[68:69], v[26:27]
	v_pk_mul_f32 v[24:25], v[66:67], v[28:29]
	s_and_saveexec_b64 s[26:27], s[0:1]
	s_cbranch_execz .LBB0_248
	v_mov_b32_e32 v26, s13
	v_mov_b32_e32 v27, s11
	v_cndmask_b32_e32 v27, v26, v27, vcc
	v_mov_b32_e32 v26, s12
	v_mov_b32_e32 v28, s10
	v_cndmask_b32_e32 v26, v26, v28, vcc
	v_lshlrev_b64 v[28:29], v80, v[90:91]
	v_lshl_add_u64 v[26:27], v[26:27], 0, v[28:29]
	v_lshl_add_u64 v[26:27], v[26:27], 0, v[146:147]
	v_mov_b64_e32 v[26:27], v[212:213]
	v_mov_b64_e32 v[28:29], v[214:215]
	v_cvt_f32_f16_e32 v32, v28
	v_cvt_f32_f16_sdwa v33, v28 dst_sel:DWORD dst_unused:UNUSED_PAD src0_sel:WORD_1
	v_cvt_f32_f16_e32 v28, v29
	v_cvt_f32_f16_sdwa v29, v29 dst_sel:DWORD dst_unused:UNUSED_PAD src0_sel:WORD_1
	v_cvt_f32_f16_e32 v30, v26
	v_cvt_f32_f16_sdwa v31, v26 dst_sel:DWORD dst_unused:UNUSED_PAD src0_sel:WORD_1
	v_cvt_f32_f16_e32 v26, v27
	v_cvt_f32_f16_sdwa v27, v27 dst_sel:DWORD dst_unused:UNUSED_PAD src0_sel:WORD_1
	v_pk_mul_f32 v[34:35], v[24:25], v[32:33]
	v_pk_mul_f32 v[36:37], v[22:23], v[28:29]
	v_pk_mul_f32 v[32:33], v[18:19], v[32:33]
	v_pk_mul_f32 v[28:29], v[20:21], v[28:29]
	v_pk_fma_f32 v[20:21], v[20:21], v[26:27], v[36:37] neg_lo:[0,0,1] neg_hi:[0,0,1]
	v_pk_fma_f32 v[18:19], v[18:19], v[30:31], v[34:35] neg_lo:[0,0,1] neg_hi:[0,0,1]
	v_pk_fma_f32 v[22:23], v[22:23], v[26:27], v[28:29]
	v_pk_fma_f32 v[24:25], v[24:25], v[30:31], v[32:33]
.LBB0_248:
	s_or_b64 exec, exec, s[26:27]
	v_cvt_pk_bf16_f32 v18, v18, v19
	v_cvt_pk_bf16_f32 v19, v20, v21
	v_cvt_pk_bf16_f32 v20, v24, v25
	v_cvt_pk_bf16_f32 v21, v22, v23
	ds_bpermute_b32 v240, v243, v84
	ds_bpermute_b32 v241, v243, v85
	ds_bpermute_b32 v244, v243, v18
	ds_bpermute_b32 v245, v243, v19
	ds_bpermute_b32 v246, v243, v20
	ds_bpermute_b32 v247, v243, v21
	s_waitcnt lgkmcnt(0)
	global_store_dwordx4 v[240:241], v[244:247], off offset:256
	s_nop 1
	v_mov_b32_e32 v18, v190
	v_cvt_f32_i32_e32 v17, v17
	v_cvt_f32_i32_e32 v16, v16
	v_cvt_f32_i32_e32 v15, v15
	v_cvt_f32_i32_e32 v14, v14
	v_cvt_f32_i32_e32 v13, v13
	v_cvt_f32_i32_e32 v11, v11
	v_cvt_f32_i32_e32 v10, v10
	v_cvt_f32_i32_e32 v12, v12
	v_pk_mul_f32 v[14:15], v[18:19], v[14:15] op_sel_hi:[0,1]
	v_pk_mul_f32 v[16:17], v[18:19], v[16:17] op_sel_hi:[0,1]
	v_pk_mul_f32 v[20:21], v[18:19], v[10:11] op_sel_hi:[0,1]
	v_pk_mul_f32 v[18:19], v[18:19], v[12:13] op_sel_hi:[0,1]
	v_pk_mul_f32 v[12:13], v[72:73], v[16:17]
	v_pk_mul_f32 v[10:11], v[70:71], v[14:15]
	v_pk_mul_f32 v[14:15], v[68:69], v[18:19]
	v_pk_mul_f32 v[16:17], v[66:67], v[20:21]
	s_and_saveexec_b64 s[26:27], s[0:1]
	s_cbranch_execz .LBB0_250
	v_mov_b32_e32 v18, s13
	v_mov_b32_e32 v19, s11
	v_cndmask_b32_e32 v19, v18, v19, vcc
	v_mov_b32_e32 v18, s12
	v_mov_b32_e32 v20, s10
	v_cndmask_b32_e32 v18, v18, v20, vcc
	v_lshlrev_b64 v[20:21], v80, v[82:83]
	v_lshl_add_u64 v[18:19], v[18:19], 0, v[20:21]
	v_lshl_add_u64 v[18:19], v[18:19], 0, v[146:147]
	v_mov_b64_e32 v[18:19], v[216:217]
	v_mov_b64_e32 v[20:21], v[218:219]
	v_cvt_f32_f16_e32 v24, v20
	v_cvt_f32_f16_sdwa v25, v20 dst_sel:DWORD dst_unused:UNUSED_PAD src0_sel:WORD_1
	v_cvt_f32_f16_e32 v20, v21
	v_cvt_f32_f16_sdwa v21, v21 dst_sel:DWORD dst_unused:UNUSED_PAD src0_sel:WORD_1
	v_cvt_f32_f16_e32 v22, v18
	v_cvt_f32_f16_sdwa v23, v18 dst_sel:DWORD dst_unused:UNUSED_PAD src0_sel:WORD_1
	v_cvt_f32_f16_e32 v18, v19
	v_cvt_f32_f16_sdwa v19, v19 dst_sel:DWORD dst_unused:UNUSED_PAD src0_sel:WORD_1
	v_pk_mul_f32 v[26:27], v[16:17], v[24:25]
	v_pk_mul_f32 v[28:29], v[14:15], v[20:21]
	v_pk_mul_f32 v[24:25], v[10:11], v[24:25]
	v_pk_mul_f32 v[20:21], v[12:13], v[20:21]
	v_pk_fma_f32 v[12:13], v[12:13], v[18:19], v[28:29] neg_lo:[0,0,1] neg_hi:[0,0,1]
	v_pk_fma_f32 v[10:11], v[10:11], v[22:23], v[26:27] neg_lo:[0,0,1] neg_hi:[0,0,1]
	v_pk_fma_f32 v[14:15], v[14:15], v[18:19], v[20:21]
	v_pk_fma_f32 v[16:17], v[16:17], v[22:23], v[24:25]
.LBB0_250:
	s_or_b64 exec, exec, s[26:27]
	v_cvt_pk_bf16_f32 v10, v10, v11
	v_cvt_pk_bf16_f32 v11, v12, v13
	v_cvt_pk_bf16_f32 v12, v16, v17
	v_cvt_pk_bf16_f32 v13, v14, v15
	ds_bpermute_b32 v240, v243, v76
	ds_bpermute_b32 v241, v243, v77
	ds_bpermute_b32 v244, v243, v10
	ds_bpermute_b32 v245, v243, v11
	ds_bpermute_b32 v246, v243, v12
	ds_bpermute_b32 v247, v243, v13
	s_waitcnt lgkmcnt(0)
	global_store_dwordx4 v[240:241], v[244:247], off offset:256
	s_nop 1
	v_mov_b32_e32 v10, v191
	v_cvt_f32_i32_e32 v9, v9
	v_cvt_f32_i32_e32 v8, v8
	v_cvt_f32_i32_e32 v7, v7
	v_cvt_f32_i32_e32 v6, v6
	v_cvt_f32_i32_e32 v5, v5
	v_cvt_f32_i32_e32 v3, v3
	v_cvt_f32_i32_e32 v2, v2
	v_cvt_f32_i32_e32 v4, v4
	v_pk_mul_f32 v[6:7], v[10:11], v[6:7] op_sel_hi:[0,1]
	v_pk_mul_f32 v[8:9], v[10:11], v[8:9] op_sel_hi:[0,1]
	v_pk_mul_f32 v[12:13], v[10:11], v[2:3] op_sel_hi:[0,1]
	v_pk_mul_f32 v[10:11], v[10:11], v[4:5] op_sel_hi:[0,1]
	v_pk_mul_f32 v[4:5], v[72:73], v[8:9]
	v_pk_mul_f32 v[2:3], v[70:71], v[6:7]
	v_pk_mul_f32 v[6:7], v[68:69], v[10:11]
	v_pk_mul_f32 v[8:9], v[66:67], v[12:13]
	s_and_saveexec_b64 s[26:27], s[0:1]
	s_cbranch_execz .LBB0_252
	v_mov_b32_e32 v10, s13
	v_mov_b32_e32 v11, s11
	v_cndmask_b32_e32 v11, v10, v11, vcc
	v_mov_b32_e32 v10, s12
	v_mov_b32_e32 v12, s10
	v_cndmask_b32_e32 v10, v10, v12, vcc
	v_lshlrev_b64 v[12:13], v80, v[74:75]
	v_lshl_add_u64 v[10:11], v[10:11], 0, v[12:13]
	v_lshl_add_u64 v[10:11], v[10:11], 0, v[146:147]
	v_mov_b64_e32 v[10:11], v[220:221]
	v_mov_b64_e32 v[12:13], v[222:223]
	v_cvt_f32_f16_e32 v16, v12
	v_cvt_f32_f16_sdwa v17, v12 dst_sel:DWORD dst_unused:UNUSED_PAD src0_sel:WORD_1
	v_cvt_f32_f16_e32 v12, v13
	v_cvt_f32_f16_sdwa v13, v13 dst_sel:DWORD dst_unused:UNUSED_PAD src0_sel:WORD_1
	v_cvt_f32_f16_e32 v14, v10
	v_cvt_f32_f16_sdwa v15, v10 dst_sel:DWORD dst_unused:UNUSED_PAD src0_sel:WORD_1
	v_cvt_f32_f16_e32 v10, v11
	v_cvt_f32_f16_sdwa v11, v11 dst_sel:DWORD dst_unused:UNUSED_PAD src0_sel:WORD_1
	v_pk_mul_f32 v[18:19], v[8:9], v[16:17]
	v_pk_mul_f32 v[20:21], v[6:7], v[12:13]
	v_pk_mul_f32 v[16:17], v[2:3], v[16:17]
	v_pk_mul_f32 v[12:13], v[4:5], v[12:13]
	v_pk_fma_f32 v[4:5], v[4:5], v[10:11], v[20:21] neg_lo:[0,0,1] neg_hi:[0,0,1]
	v_pk_fma_f32 v[2:3], v[2:3], v[14:15], v[18:19] neg_lo:[0,0,1] neg_hi:[0,0,1]
	v_pk_fma_f32 v[6:7], v[6:7], v[10:11], v[12:13]
	v_pk_fma_f32 v[8:9], v[8:9], v[14:15], v[16:17]
.LBB0_252:
	s_or_b64 exec, exec, s[26:27]
	s_andn2_b64 vcc, exec, s[2:3]
	s_mov_b64 s[0:1], -1
	v_cvt_pk_bf16_f32 v2, v2, v3
	v_cvt_pk_bf16_f32 v3, v4, v5
	v_cvt_pk_bf16_f32 v4, v8, v9
	v_cvt_pk_bf16_f32 v5, v6, v7
	ds_bpermute_b32 v240, v243, v78
	ds_bpermute_b32 v241, v243, v79
	ds_bpermute_b32 v244, v243, v2
	ds_bpermute_b32 v245, v243, v3
	ds_bpermute_b32 v246, v243, v4
	ds_bpermute_b32 v247, v243, v5
	s_waitcnt lgkmcnt(0)
	global_store_dwordx4 v[240:241], v[244:247], off offset:256
	s_cbranch_vccnz .LBB0_213
	s_andn2_b64 vcc, exec, s[6:7]
	s_cbranch_vccnz .LBB0_212
	s_barrier
	s_branch .LBB0_212

.LBB0_1235:
	v_mbcnt_lo_u32_b32 v243, -1, 0
	v_mbcnt_hi_u32_b32 v243, -1, v243
	v_lshrrev_b32_e32 v244, 2, v243
	v_and_b32_e32 v243, 3, v243
	v_lshl_add_u32 v243, v243, 4, v244
	v_lshlrev_b32_e32 v243, 2, v243
	s_ashr_i32 s19, s26, 31
	s_lshr_b32 s19, s19, 28
	s_add_i32 s19, s26, s19
	s_ashr_i32 s19, s19, 4
	s_mul_hi_i32 s21, s19, 0x18000
	s_mul_i32 s19, s19, 0x18000
	s_add_u32 s19, s78, s19
	v_lshl_or_b32 v146, s56, 8, v157
	s_addc_u32 s21, s79, s21
	s_add_u32 s30, s19, 0x8000
	v_ashrrev_i32_e32 v147, 31, v146
	v_lshl_add_u32 v154, s26, 8, v1
	s_addc_u32 s31, s21, 0
	v_lshlrev_b64 v[150:151], 2, v[146:147]
	v_ashrrev_i32_e32 v155, 31, v154
	v_lshl_add_u64 v[152:153], s[30:31], 0, v[150:151]
	v_lshl_add_u64 v[148:149], v[154:155], 2, s[72:73]
	v_lshl_add_u64 v[150:151], s[6:7], 0, v[150:151]
	v_readlane_b32 s80, v242, 11
	global_load_dword v174, v[148:149], off
	global_load_dwordx4 v[162:165], v[152:153], off offset:16
	global_load_dwordx4 v[166:169], v[152:153], off
	global_load_dwordx4 v[170:173], v[150:151], off offset:16
	global_load_dwordx4 v[176:179], v[150:151], off
	v_lshlrev_b64 v[150:151], 12, v[154:155]
	v_readlane_b32 s81, v242, 12
	v_lshl_add_u64 v[152:153], v[150:151], 0, v[146:147]
	s_mov_b64 s[56:57], s[80:81]
	v_lshl_add_u64 v[204:205], v[152:153], 2, s[56:57]
	global_load_dwordx4 v[180:183], v[204:205], off
	global_load_dwordx4 v[184:187], v[204:205], off offset:16
	v_cvt_f32_i32_e32 v129, v129
	v_cvt_f32_i32_e32 v128, v128
	v_cvt_f32_i32_e32 v127, v127
	v_cvt_f32_i32_e32 v126, v126
	v_cvt_f32_i32_e32 v125, v125
	v_cvt_f32_i32_e32 v124, v124
	v_cvt_f32_i32_e32 v207, v123
	v_cvt_f32_i32_e32 v206, v122
	v_or_b32_e32 v122, 0x80, v146
	v_ashrrev_i32_e32 v123, 31, v122
	v_lshlrev_b64 v[196:197], 2, v[122:123]
	v_lshl_add_u64 v[192:193], s[6:7], 0, v[196:197]
	v_lshl_add_u64 v[208:209], v[152:153], 1, s[28:29]
	v_lshl_add_u64 v[152:153], s[30:31], 0, v[196:197]
	global_load_dwordx4 v[188:191], v[192:193], off offset:16
	s_nop 0
	global_load_dwordx4 v[192:195], v[192:193], off
	s_nop 0
	global_load_dwordx4 v[196:199], v[152:153], off offset:16
	global_load_dwordx4 v[200:203], v[152:153], off
	v_cvt_f32_i32_e32 v121, v121
	v_cvt_f32_i32_e32 v120, v120
	v_cvt_f32_i32_e32 v119, v119
	v_cvt_f32_i32_e32 v118, v118
	v_cvt_f32_i32_e32 v117, v117
	v_cvt_f32_i32_e32 v116, v116
	v_cvt_f32_i32_e32 v115, v115
	v_cvt_f32_i32_e32 v114, v114
	v_mov_b32_e32 v123, v147
	v_cvt_f32_i32_e32 v111, v111
	v_cvt_f32_i32_e32 v110, v110
	v_cvt_f32_i32_e32 v109, v109
	v_cvt_f32_i32_e32 v108, v108
	v_cvt_f32_i32_e32 v107, v107
	v_cvt_f32_i32_e32 v106, v106
	v_cvt_f32_i32_e32 v113, v113
	v_cvt_f32_i32_e32 v112, v112
	v_cvt_f32_i32_e32 v105, v105
	v_cvt_f32_i32_e32 v104, v104
	v_cvt_f32_i32_e32 v103, v103
	v_cvt_f32_i32_e32 v102, v102
	v_cvt_f32_i32_e32 v101, v101
	v_cvt_f32_i32_e32 v100, v100
	v_cvt_f32_i32_e32 v99, v99
	v_cvt_f32_i32_e32 v98, v98
	v_cvt_f32_i32_e32 v95, v95
	v_cvt_f32_i32_e32 v94, v94
	v_cvt_f32_i32_e32 v93, v93
	v_cvt_f32_i32_e32 v92, v92
	v_cvt_f32_i32_e32 v91, v91
	v_cvt_f32_i32_e32 v90, v90
	v_cvt_f32_i32_e32 v97, v97
	v_cvt_f32_i32_e32 v96, v96
	v_cvt_f32_i32_e32 v89, v89
	v_cvt_f32_i32_e32 v88, v88
	v_cvt_f32_i32_e32 v87, v87
	v_cvt_f32_i32_e32 v86, v86
	v_cvt_f32_i32_e32 v85, v85
	v_cvt_f32_i32_e32 v84, v84
	v_cvt_f32_i32_e32 v83, v83
	v_cvt_f32_i32_e32 v82, v82
	v_cvt_f32_i32_e32 v79, v79
	v_cvt_f32_i32_e32 v78, v78
	v_cvt_f32_i32_e32 v77, v77
	v_cvt_f32_i32_e32 v76, v76
	v_cvt_f32_i32_e32 v75, v75
	v_cvt_f32_i32_e32 v74, v74
	v_cvt_f32_i32_e32 v81, v81
	v_cvt_f32_i32_e32 v80, v80
	v_cvt_f32_i32_e32 v73, v73
	v_cvt_f32_i32_e32 v72, v72
	v_cvt_f32_i32_e32 v71, v71
	v_cvt_f32_i32_e32 v70, v70
	v_cvt_f32_i32_e32 v69, v69
	s_waitcnt vmcnt(0)
	v_pk_mul_f32 v[210:211], v[174:175], v[126:127] op_sel_hi:[0,1]
	v_pk_mul_f32 v[212:213], v[174:175], v[128:129] op_sel_hi:[0,1]
	v_pk_mul_f32 v[214:215], v[174:175], v[124:125] op_sel_hi:[0,1]
	v_pk_mul_f32 v[124:125], v[168:169], v[178:179]
	v_pk_mul_f32 v[126:127], v[166:167], v[176:177]
	v_pk_mul_f32 v[206:207], v[174:175], v[206:207] op_sel_hi:[0,1]
	v_pk_mul_f32 v[128:129], v[164:165], v[172:173]
	v_pk_mul_f32 v[152:153], v[162:163], v[170:171]
	v_pk_fma_f32 v[164:165], v[124:125], v[212:213], v[182:183]
	v_pk_fma_f32 v[162:163], v[126:127], v[210:211], v[180:181]
	v_pk_fma_f32 v[166:167], v[128:129], v[214:215], v[186:187]
	v_pk_fma_f32 v[168:169], v[152:153], v[206:207], v[184:185]
	v_cvt_pk_bf16_f32 v162, v162, v163
	v_cvt_pk_bf16_f32 v163, v164, v165
	v_or_b32_e32 v170, 16, v154
	v_cvt_pk_bf16_f32 v164, v168, v169
	v_cvt_pk_bf16_f32 v165, v166, v167
	ds_bpermute_b32 v240, v243, v208
	ds_bpermute_b32 v241, v243, v209
	ds_bpermute_b32 v244, v243, v162
	ds_bpermute_b32 v245, v243, v163
	ds_bpermute_b32 v246, v243, v164
	ds_bpermute_b32 v247, v243, v165
	s_waitcnt lgkmcnt(0)
	global_store_dwordx4 v[240:241], v[244:247], off
	global_load_dwordx4 v[162:165], v[204:205], off offset:512
	s_nop 0
	global_load_dwordx4 v[166:169], v[204:205], off offset:528
	v_ashrrev_i32_e32 v171, 31, v170
	v_lshl_add_u64 v[176:177], v[150:151], 0, v[122:123]
	v_pk_mul_f32 v[178:179], v[174:175], v[118:119] op_sel_hi:[0,1]
	v_pk_mul_f32 v[180:181], v[174:175], v[120:121] op_sel_hi:[0,1]
	v_pk_mul_f32 v[182:183], v[174:175], v[114:115] op_sel_hi:[0,1]
	v_pk_mul_f32 v[184:185], v[174:175], v[116:117] op_sel_hi:[0,1]
	v_pk_mul_f32 v[114:115], v[202:203], v[194:195]
	v_pk_mul_f32 v[116:117], v[200:201], v[192:193]
	v_lshl_add_u64 v[172:173], v[170:171], 2, s[72:73]
	v_lshl_add_u64 v[176:177], v[176:177], 1, s[28:29]
	v_pk_mul_f32 v[118:119], v[198:199], v[190:191]
	v_pk_mul_f32 v[120:121], v[196:197], v[188:189]
	v_lshlrev_b64 v[170:171], 12, v[170:171]
	v_cvt_f32_i32_e32 v68, v68
	v_cvt_f32_i32_e32 v67, v67
	v_cvt_f32_i32_e32 v66, v66
	s_mov_b64 s[30:31], 0x80000
	v_cvt_f32_i32_e32 v63, v63
	v_cvt_f32_i32_e32 v62, v62
	v_cvt_f32_i32_e32 v61, v61
	v_cvt_f32_i32_e32 v60, v60
	v_cvt_f32_i32_e32 v59, v59
	v_cvt_f32_i32_e32 v58, v58
	v_cvt_f32_i32_e32 v65, v65
	v_cvt_f32_i32_e32 v64, v64
	v_cvt_f32_i32_e32 v57, v57
	v_cvt_f32_i32_e32 v56, v56
	v_cvt_f32_i32_e32 v55, v55
	v_cvt_f32_i32_e32 v54, v54
	v_cvt_f32_i32_e32 v53, v53
	v_cvt_f32_i32_e32 v52, v52
	v_cvt_f32_i32_e32 v51, v51
	v_cvt_f32_i32_e32 v50, v50
	v_cvt_f32_i32_e32 v47, v47
	v_cvt_f32_i32_e32 v46, v46
	v_cvt_f32_i32_e32 v45, v45
	v_cvt_f32_i32_e32 v44, v44
	v_cvt_f32_i32_e32 v43, v43
	v_cvt_f32_i32_e32 v42, v42
	v_cvt_f32_i32_e32 v49, v49
	v_cvt_f32_i32_e32 v48, v48
	v_cvt_f32_i32_e32 v41, v41
	v_cvt_f32_i32_e32 v40, v40
	v_cvt_f32_i32_e32 v39, v39
	v_cvt_f32_i32_e32 v38, v38
	v_cvt_f32_i32_e32 v37, v37
	v_cvt_f32_i32_e32 v36, v36
	v_cvt_f32_i32_e32 v35, v35
	v_cvt_f32_i32_e32 v34, v34
	v_cvt_f32_i32_e32 v31, v31
	v_cvt_f32_i32_e32 v30, v30
	v_cvt_f32_i32_e32 v29, v29
	v_cvt_f32_i32_e32 v28, v28
	v_cvt_f32_i32_e32 v27, v27
	v_cvt_f32_i32_e32 v26, v26
	v_cvt_f32_i32_e32 v33, v33
	v_cvt_f32_i32_e32 v32, v32
	v_cvt_f32_i32_e32 v25, v25
	v_cvt_f32_i32_e32 v24, v24
	v_cvt_f32_i32_e32 v23, v23
	v_cvt_f32_i32_e32 v22, v22
	v_cvt_f32_i32_e32 v21, v21
	v_cvt_f32_i32_e32 v20, v20
	v_cvt_f32_i32_e32 v19, v19
	v_cvt_f32_i32_e32 v18, v18
	v_cvt_f32_i32_e32 v15, v15
	v_cvt_f32_i32_e32 v14, v14
	v_cvt_f32_i32_e32 v13, v13
	v_cvt_f32_i32_e32 v12, v12
	v_cvt_f32_i32_e32 v11, v11
	v_cvt_f32_i32_e32 v10, v10
	v_cvt_f32_i32_e32 v17, v17
	v_cvt_f32_i32_e32 v16, v16
	v_cvt_f32_i32_e32 v7, v7
	v_cvt_f32_i32_e32 v6, v6
	v_cvt_f32_i32_e32 v5, v5
	v_cvt_f32_i32_e32 v4, v4
	v_cvt_f32_i32_e32 v3, v3
	s_waitcnt vmcnt(1)
	v_pk_fma_f32 v[164:165], v[114:115], v[180:181], v[164:165]
	v_pk_fma_f32 v[162:163], v[116:117], v[178:179], v[162:163]
	s_waitcnt vmcnt(0)
	v_pk_fma_f32 v[168:169], v[118:119], v[184:185], v[168:169]
	v_pk_fma_f32 v[166:167], v[120:121], v[182:183], v[166:167]
	v_cvt_pk_bf16_f32 v162, v162, v163
	v_cvt_pk_bf16_f32 v163, v164, v165
	v_cvt_f32_i32_e32 v2, v2
	v_cvt_pk_bf16_f32 v164, v166, v167
	v_cvt_pk_bf16_f32 v165, v168, v169
	ds_bpermute_b32 v240, v243, v176
	ds_bpermute_b32 v241, v243, v177
	ds_bpermute_b32 v244, v243, v162
	ds_bpermute_b32 v245, v243, v163
	ds_bpermute_b32 v246, v243, v164
	ds_bpermute_b32 v247, v243, v165
	s_waitcnt lgkmcnt(0)
	global_store_dwordx4 v[240:241], v[244:247], off
	v_lshl_add_u64 v[176:177], v[170:171], 0, v[146:147]
	global_load_dword v172, v[172:173], off
	v_lshl_add_u64 v[178:179], v[176:177], 2, s[56:57]
	global_load_dwordx4 v[162:165], v[178:179], off
	global_load_dwordx4 v[166:169], v[178:179], off offset:16
	v_lshl_add_u64 v[176:177], v[176:177], 1, s[28:29]
	v_cvt_f32_i32_e32 v9, v9
	v_cvt_f32_i32_e32 v8, v8
	s_andn2_b64 vcc, exec, s[2:3]
	s_mov_b64 s[2:3], -1
	v_readlane_b32 s82, v242, 13
	v_readlane_b32 s83, v242, 14
	v_readlane_b32 s84, v242, 15
	v_readlane_b32 s85, v242, 16
	v_readlane_b32 s86, v242, 17
	v_readlane_b32 s87, v242, 18
	v_readlane_b32 s88, v242, 19
	v_readlane_b32 s89, v242, 20
	v_readlane_b32 s90, v242, 21
	v_readlane_b32 s91, v242, 22
	v_readlane_b32 s92, v242, 23
	v_readlane_b32 s93, v242, 24
	v_readlane_b32 s94, v242, 25
	v_readlane_b32 s95, v242, 26
	s_waitcnt vmcnt(2)
	v_pk_mul_f32 v[110:111], v[172:173], v[110:111] op_sel_hi:[0,1]
	v_pk_mul_f32 v[106:107], v[172:173], v[106:107] op_sel_hi:[0,1]
	v_pk_mul_f32 v[108:109], v[172:173], v[108:109] op_sel_hi:[0,1]
	v_pk_mul_f32 v[112:113], v[172:173], v[112:113] op_sel_hi:[0,1]
	s_waitcnt vmcnt(1)
	v_pk_fma_f32 v[110:111], v[126:127], v[110:111], v[162:163]
	s_waitcnt vmcnt(0)
	v_pk_fma_f32 v[162:163], v[128:129], v[108:109], v[168:169]
	v_pk_fma_f32 v[108:109], v[152:153], v[106:107], v[166:167]
	v_pk_fma_f32 v[112:113], v[124:125], v[112:113], v[164:165]
	v_cvt_pk_bf16_f32 v106, v110, v111
	v_lshl_add_u64 v[166:167], v[170:171], 0, v[122:123]
	v_cvt_pk_bf16_f32 v107, v112, v113
	v_cvt_pk_bf16_f32 v108, v108, v109
	v_cvt_pk_bf16_f32 v109, v162, v163
	ds_bpermute_b32 v240, v243, v176
	ds_bpermute_b32 v241, v243, v177
	ds_bpermute_b32 v244, v243, v106
	ds_bpermute_b32 v245, v243, v107
	ds_bpermute_b32 v246, v243, v108
	ds_bpermute_b32 v247, v243, v109
	s_waitcnt lgkmcnt(0)
	global_store_dwordx4 v[240:241], v[244:247], off
	global_load_dwordx4 v[106:109], v[178:179], off offset:512
	s_nop 0
	global_load_dwordx4 v[110:113], v[178:179], off offset:528
	v_or_b32_e32 v162, 32, v154
	v_ashrrev_i32_e32 v163, 31, v162
	v_pk_mul_f32 v[102:103], v[172:173], v[102:103] op_sel_hi:[0,1]
	v_pk_mul_f32 v[104:105], v[172:173], v[104:105] op_sel_hi:[0,1]
	v_pk_mul_f32 v[98:99], v[172:173], v[98:99] op_sel_hi:[0,1]
	v_pk_mul_f32 v[100:101], v[172:173], v[100:101] op_sel_hi:[0,1]
	v_lshl_add_u64 v[166:167], v[166:167], 1, s[28:29]
	v_lshl_add_u64 v[164:165], v[162:163], 2, s[72:73]
	s_waitcnt vmcnt(1)
	v_pk_fma_f32 v[104:105], v[114:115], v[104:105], v[108:109]
	v_pk_fma_f32 v[102:103], v[116:117], v[102:103], v[106:107]
	s_waitcnt vmcnt(0)
	v_pk_fma_f32 v[106:107], v[118:119], v[100:101], v[112:113]
	v_pk_fma_f32 v[100:101], v[120:121], v[98:99], v[110:111]
	v_lshlrev_b64 v[108:109], 12, v[162:163]
	v_cvt_pk_bf16_f32 v98, v102, v103
	v_cvt_pk_bf16_f32 v99, v104, v105
	v_cvt_pk_bf16_f32 v100, v100, v101
	v_cvt_pk_bf16_f32 v101, v106, v107
	ds_bpermute_b32 v240, v243, v166
	ds_bpermute_b32 v241, v243, v167
	ds_bpermute_b32 v244, v243, v98
	ds_bpermute_b32 v245, v243, v99
	ds_bpermute_b32 v246, v243, v100
	ds_bpermute_b32 v247, v243, v101
	s_waitcnt lgkmcnt(0)
	global_store_dwordx4 v[240:241], v[244:247], off
	v_lshl_add_u64 v[110:111], v[108:109], 0, v[146:147]
	global_load_dword v106, v[164:165], off
	v_lshl_add_u64 v[112:113], v[110:111], 2, s[56:57]
	global_load_dwordx4 v[98:101], v[112:113], off
	global_load_dwordx4 v[102:105], v[112:113], off offset:16
	v_lshl_add_u64 v[110:111], v[110:111], 1, s[28:29]
	s_waitcnt vmcnt(2)
	v_pk_mul_f32 v[94:95], v[106:107], v[94:95] op_sel_hi:[0,1]
	v_pk_mul_f32 v[90:91], v[106:107], v[90:91] op_sel_hi:[0,1]
	v_pk_mul_f32 v[92:93], v[106:107], v[92:93] op_sel_hi:[0,1]
	v_pk_mul_f32 v[96:97], v[106:107], v[96:97] op_sel_hi:[0,1]
	s_waitcnt vmcnt(1)
	v_pk_fma_f32 v[94:95], v[126:127], v[94:95], v[98:99]
	s_waitcnt vmcnt(0)
	v_pk_fma_f32 v[98:99], v[128:129], v[92:93], v[104:105]
	v_pk_fma_f32 v[92:93], v[152:153], v[90:91], v[102:103]
	v_pk_fma_f32 v[96:97], v[124:125], v[96:97], v[100:101]
	v_cvt_pk_bf16_f32 v90, v94, v95
	v_lshl_add_u64 v[102:103], v[108:109], 0, v[122:123]
	v_cvt_pk_bf16_f32 v91, v96, v97
	v_cvt_pk_bf16_f32 v92, v92, v93
	v_cvt_pk_bf16_f32 v93, v98, v99
	ds_bpermute_b32 v240, v243, v110
	ds_bpermute_b32 v241, v243, v111
	ds_bpermute_b32 v244, v243, v90
	ds_bpermute_b32 v245, v243, v91
	ds_bpermute_b32 v246, v243, v92
	ds_bpermute_b32 v247, v243, v93
	s_waitcnt lgkmcnt(0)
	global_store_dwordx4 v[240:241], v[244:247], off
	global_load_dwordx4 v[90:93], v[112:113], off offset:512
	s_nop 0
	global_load_dwordx4 v[94:97], v[112:113], off offset:528
	v_or_b32_e32 v98, 48, v154
	v_ashrrev_i32_e32 v99, 31, v98
	v_pk_mul_f32 v[86:87], v[106:107], v[86:87] op_sel_hi:[0,1]
	v_pk_mul_f32 v[88:89], v[106:107], v[88:89] op_sel_hi:[0,1]
	v_pk_mul_f32 v[82:83], v[106:107], v[82:83] op_sel_hi:[0,1]
	v_pk_mul_f32 v[84:85], v[106:107], v[84:85] op_sel_hi:[0,1]
	v_lshl_add_u64 v[102:103], v[102:103], 1, s[28:29]
	v_lshl_add_u64 v[100:101], v[98:99], 2, s[72:73]
	s_waitcnt vmcnt(1)
	v_pk_fma_f32 v[88:89], v[114:115], v[88:89], v[92:93]
	v_pk_fma_f32 v[86:87], v[116:117], v[86:87], v[90:91]
	s_waitcnt vmcnt(0)
	v_pk_fma_f32 v[90:91], v[118:119], v[84:85], v[96:97]
	v_pk_fma_f32 v[84:85], v[120:121], v[82:83], v[94:95]
	v_lshlrev_b64 v[92:93], 12, v[98:99]
	v_cvt_pk_bf16_f32 v82, v86, v87
	v_cvt_pk_bf16_f32 v83, v88, v89
	v_cvt_pk_bf16_f32 v84, v84, v85
	v_cvt_pk_bf16_f32 v85, v90, v91
	ds_bpermute_b32 v240, v243, v102
	ds_bpermute_b32 v241, v243, v103
	ds_bpermute_b32 v244, v243, v82
	ds_bpermute_b32 v245, v243, v83
	ds_bpermute_b32 v246, v243, v84
	ds_bpermute_b32 v247, v243, v85
	s_waitcnt lgkmcnt(0)
	global_store_dwordx4 v[240:241], v[244:247], off
	v_lshl_add_u64 v[94:95], v[92:93], 0, v[146:147]
	global_load_dword v90, v[100:101], off
	v_lshl_add_u64 v[96:97], v[94:95], 2, s[56:57]
	global_load_dwordx4 v[82:85], v[96:97], off
	global_load_dwordx4 v[86:89], v[96:97], off offset:16
	v_lshl_add_u64 v[94:95], v[94:95], 1, s[28:29]
	s_waitcnt vmcnt(2)
	v_pk_mul_f32 v[78:79], v[90:91], v[78:79] op_sel_hi:[0,1]
	v_pk_mul_f32 v[74:75], v[90:91], v[74:75] op_sel_hi:[0,1]
	v_pk_mul_f32 v[76:77], v[90:91], v[76:77] op_sel_hi:[0,1]
	v_pk_mul_f32 v[80:81], v[90:91], v[80:81] op_sel_hi:[0,1]
	s_waitcnt vmcnt(1)
	v_pk_fma_f32 v[78:79], v[126:127], v[78:79], v[82:83]
	s_waitcnt vmcnt(0)
	v_pk_fma_f32 v[82:83], v[128:129], v[76:77], v[88:89]
	v_pk_fma_f32 v[76:77], v[152:153], v[74:75], v[86:87]
	v_pk_fma_f32 v[80:81], v[124:125], v[80:81], v[84:85]
	v_cvt_pk_bf16_f32 v74, v78, v79
	v_pk_mul_f32 v[70:71], v[90:91], v[70:71] op_sel_hi:[0,1]
	v_cvt_pk_bf16_f32 v75, v80, v81
	v_cvt_pk_bf16_f32 v76, v76, v77
	v_cvt_pk_bf16_f32 v77, v82, v83
	ds_bpermute_b32 v240, v243, v94
	ds_bpermute_b32 v241, v243, v95
	ds_bpermute_b32 v244, v243, v74
	ds_bpermute_b32 v245, v243, v75
	ds_bpermute_b32 v246, v243, v76
	ds_bpermute_b32 v247, v243, v77
	s_waitcnt lgkmcnt(0)
	global_store_dwordx4 v[240:241], v[244:247], off
	global_load_dwordx4 v[74:77], v[96:97], off offset:512
	s_nop 0
	global_load_dwordx4 v[78:81], v[96:97], off offset:528
	v_lshl_add_u64 v[82:83], v[92:93], 0, v[122:123]
	v_pk_mul_f32 v[72:73], v[90:91], v[72:73] op_sel_hi:[0,1]
	v_pk_mul_f32 v[66:67], v[90:91], v[66:67] op_sel_hi:[0,1]
	v_pk_mul_f32 v[68:69], v[90:91], v[68:69] op_sel_hi:[0,1]
	v_lshl_add_u64 v[82:83], v[82:83], 1, s[28:29]
	s_waitcnt vmcnt(1)
	v_pk_fma_f32 v[72:73], v[114:115], v[72:73], v[76:77]
	v_pk_fma_f32 v[70:71], v[116:117], v[70:71], v[74:75]
	s_waitcnt vmcnt(0)
	v_pk_fma_f32 v[74:75], v[118:119], v[68:69], v[80:81]
	v_pk_fma_f32 v[68:69], v[120:121], v[66:67], v[78:79]
	v_lshl_add_u64 v[76:77], v[150:151], 0, s[30:31]
	v_cvt_pk_bf16_f32 v66, v70, v71
	v_cvt_pk_bf16_f32 v67, v72, v73
	v_cvt_pk_bf16_f32 v68, v68, v69
	v_cvt_pk_bf16_f32 v69, v74, v75
	ds_bpermute_b32 v240, v243, v82
	ds_bpermute_b32 v241, v243, v83
	ds_bpermute_b32 v244, v243, v66
	ds_bpermute_b32 v245, v243, v67
	ds_bpermute_b32 v246, v243, v68
	ds_bpermute_b32 v247, v243, v69
	s_waitcnt lgkmcnt(0)
	global_store_dwordx4 v[240:241], v[244:247], off
	v_lshl_add_u64 v[78:79], v[76:77], 0, v[146:147]
	global_load_dword v74, v[148:149], off offset:512
	v_lshl_add_u64 v[80:81], v[78:79], 2, s[56:57]
	global_load_dwordx4 v[66:69], v[80:81], off
	global_load_dwordx4 v[70:73], v[80:81], off offset:16
	v_lshl_add_u64 v[78:79], v[78:79], 1, s[28:29]
	s_waitcnt vmcnt(2)
	v_pk_mul_f32 v[62:63], v[74:75], v[62:63] op_sel_hi:[0,1]
	v_pk_mul_f32 v[58:59], v[74:75], v[58:59] op_sel_hi:[0,1]
	v_pk_mul_f32 v[60:61], v[74:75], v[60:61] op_sel_hi:[0,1]
	v_pk_mul_f32 v[64:65], v[74:75], v[64:65] op_sel_hi:[0,1]
	s_waitcnt vmcnt(1)
	v_pk_fma_f32 v[62:63], v[126:127], v[62:63], v[66:67]
	s_waitcnt vmcnt(0)
	v_pk_fma_f32 v[66:67], v[128:129], v[60:61], v[72:73]
	v_pk_fma_f32 v[60:61], v[152:153], v[58:59], v[70:71]
	v_pk_fma_f32 v[64:65], v[124:125], v[64:65], v[68:69]
	v_cvt_pk_bf16_f32 v58, v62, v63
	v_pk_mul_f32 v[54:55], v[74:75], v[54:55] op_sel_hi:[0,1]
	v_cvt_pk_bf16_f32 v59, v64, v65
	v_cvt_pk_bf16_f32 v60, v60, v61
	v_cvt_pk_bf16_f32 v61, v66, v67
	ds_bpermute_b32 v240, v243, v78
	ds_bpermute_b32 v241, v243, v79
	ds_bpermute_b32 v244, v243, v58
	ds_bpermute_b32 v245, v243, v59
	ds_bpermute_b32 v246, v243, v60
	ds_bpermute_b32 v247, v243, v61
	s_waitcnt lgkmcnt(0)
	global_store_dwordx4 v[240:241], v[244:247], off
	global_load_dwordx4 v[58:61], v[80:81], off offset:512
	s_nop 0
	global_load_dwordx4 v[62:65], v[80:81], off offset:528
	v_lshl_add_u64 v[66:67], v[76:77], 0, v[122:123]
	v_pk_mul_f32 v[56:57], v[74:75], v[56:57] op_sel_hi:[0,1]
	v_pk_mul_f32 v[50:51], v[74:75], v[50:51] op_sel_hi:[0,1]
	v_pk_mul_f32 v[52:53], v[74:75], v[52:53] op_sel_hi:[0,1]
	v_lshl_add_u64 v[66:67], v[66:67], 1, s[28:29]
	s_waitcnt vmcnt(1)
	v_pk_fma_f32 v[56:57], v[114:115], v[56:57], v[60:61]
	v_pk_fma_f32 v[54:55], v[116:117], v[54:55], v[58:59]
	s_waitcnt vmcnt(0)
	v_pk_fma_f32 v[58:59], v[118:119], v[52:53], v[64:65]
	v_pk_fma_f32 v[52:53], v[120:121], v[50:51], v[62:63]
	v_lshl_add_u64 v[60:61], v[150:151], 0, s[12:13]
	v_cvt_pk_bf16_f32 v50, v54, v55
	v_cvt_pk_bf16_f32 v51, v56, v57
	v_cvt_pk_bf16_f32 v52, v52, v53
	v_cvt_pk_bf16_f32 v53, v58, v59
	ds_bpermute_b32 v240, v243, v66
	ds_bpermute_b32 v241, v243, v67
	ds_bpermute_b32 v244, v243, v50
	ds_bpermute_b32 v245, v243, v51
	ds_bpermute_b32 v246, v243, v52
	ds_bpermute_b32 v247, v243, v53
	s_waitcnt lgkmcnt(0)
	global_store_dwordx4 v[240:241], v[244:247], off
	v_lshl_add_u64 v[62:63], v[60:61], 0, v[146:147]
	global_load_dword v58, v[148:149], off offset:576
	v_lshl_add_u64 v[64:65], v[62:63], 2, s[56:57]
	global_load_dwordx4 v[50:53], v[64:65], off
	global_load_dwordx4 v[54:57], v[64:65], off offset:16
	v_lshl_add_u64 v[62:63], v[62:63], 1, s[28:29]
	s_waitcnt vmcnt(2)
	v_pk_mul_f32 v[46:47], v[58:59], v[46:47] op_sel_hi:[0,1]
	v_pk_mul_f32 v[42:43], v[58:59], v[42:43] op_sel_hi:[0,1]
	v_pk_mul_f32 v[44:45], v[58:59], v[44:45] op_sel_hi:[0,1]
	v_pk_mul_f32 v[48:49], v[58:59], v[48:49] op_sel_hi:[0,1]
	s_waitcnt vmcnt(1)
	v_pk_fma_f32 v[46:47], v[126:127], v[46:47], v[50:51]
	s_waitcnt vmcnt(0)
	v_pk_fma_f32 v[50:51], v[128:129], v[44:45], v[56:57]
	v_pk_fma_f32 v[44:45], v[152:153], v[42:43], v[54:55]
	v_pk_fma_f32 v[48:49], v[124:125], v[48:49], v[52:53]
	v_cvt_pk_bf16_f32 v42, v46, v47
	v_pk_mul_f32 v[38:39], v[58:59], v[38:39] op_sel_hi:[0,1]
	v_cvt_pk_bf16_f32 v43, v48, v49
	v_cvt_pk_bf16_f32 v44, v44, v45
	v_cvt_pk_bf16_f32 v45, v50, v51
	ds_bpermute_b32 v240, v243, v62
	ds_bpermute_b32 v241, v243, v63
	ds_bpermute_b32 v244, v243, v42
	ds_bpermute_b32 v245, v243, v43
	ds_bpermute_b32 v246, v243, v44
	ds_bpermute_b32 v247, v243, v45
	s_waitcnt lgkmcnt(0)
	global_store_dwordx4 v[240:241], v[244:247], off
	global_load_dwordx4 v[42:45], v[64:65], off offset:512
	s_nop 0
	global_load_dwordx4 v[46:49], v[64:65], off offset:528
	v_lshl_add_u64 v[50:51], v[60:61], 0, v[122:123]
	v_pk_mul_f32 v[40:41], v[58:59], v[40:41] op_sel_hi:[0,1]
	v_pk_mul_f32 v[34:35], v[58:59], v[34:35] op_sel_hi:[0,1]
	v_pk_mul_f32 v[36:37], v[58:59], v[36:37] op_sel_hi:[0,1]
	v_lshl_add_u64 v[50:51], v[50:51], 1, s[28:29]
	s_waitcnt vmcnt(1)
	v_pk_fma_f32 v[40:41], v[114:115], v[40:41], v[44:45]
	v_pk_fma_f32 v[38:39], v[116:117], v[38:39], v[42:43]
	s_waitcnt vmcnt(0)
	v_pk_fma_f32 v[42:43], v[118:119], v[36:37], v[48:49]
	v_pk_fma_f32 v[36:37], v[120:121], v[34:35], v[46:47]
	v_lshl_add_u64 v[44:45], v[150:151], 0, s[14:15]
	v_cvt_pk_bf16_f32 v34, v38, v39
	v_cvt_pk_bf16_f32 v35, v40, v41
	v_cvt_pk_bf16_f32 v36, v36, v37
	v_cvt_pk_bf16_f32 v37, v42, v43
	ds_bpermute_b32 v240, v243, v50
	ds_bpermute_b32 v241, v243, v51
	ds_bpermute_b32 v244, v243, v34
	ds_bpermute_b32 v245, v243, v35
	ds_bpermute_b32 v246, v243, v36
	ds_bpermute_b32 v247, v243, v37
	s_waitcnt lgkmcnt(0)
	global_store_dwordx4 v[240:241], v[244:247], off
	v_lshl_add_u64 v[46:47], v[44:45], 0, v[146:147]
	global_load_dword v42, v[148:149], off offset:640
	v_lshl_add_u64 v[48:49], v[46:47], 2, s[56:57]
	global_load_dwordx4 v[34:37], v[48:49], off
	global_load_dwordx4 v[38:41], v[48:49], off offset:16
	v_lshl_add_u64 v[46:47], v[46:47], 1, s[28:29]
	s_waitcnt vmcnt(2)
	v_pk_mul_f32 v[30:31], v[42:43], v[30:31] op_sel_hi:[0,1]
	v_pk_mul_f32 v[26:27], v[42:43], v[26:27] op_sel_hi:[0,1]
	v_pk_mul_f32 v[28:29], v[42:43], v[28:29] op_sel_hi:[0,1]
	v_pk_mul_f32 v[32:33], v[42:43], v[32:33] op_sel_hi:[0,1]
	s_waitcnt vmcnt(1)
	v_pk_fma_f32 v[30:31], v[126:127], v[30:31], v[34:35]
	s_waitcnt vmcnt(0)
	v_pk_fma_f32 v[34:35], v[128:129], v[28:29], v[40:41]
	v_pk_fma_f32 v[28:29], v[152:153], v[26:27], v[38:39]
	v_pk_fma_f32 v[32:33], v[124:125], v[32:33], v[36:37]
	v_cvt_pk_bf16_f32 v26, v30, v31
	v_pk_mul_f32 v[22:23], v[42:43], v[22:23] op_sel_hi:[0,1]
	v_cvt_pk_bf16_f32 v27, v32, v33
	v_cvt_pk_bf16_f32 v28, v28, v29
	v_cvt_pk_bf16_f32 v29, v34, v35
	ds_bpermute_b32 v240, v243, v46
	ds_bpermute_b32 v241, v243, v47
	ds_bpermute_b32 v244, v243, v26
	ds_bpermute_b32 v245, v243, v27
	ds_bpermute_b32 v246, v243, v28
	ds_bpermute_b32 v247, v243, v29
	s_waitcnt lgkmcnt(0)
	global_store_dwordx4 v[240:241], v[244:247], off
	global_load_dwordx4 v[26:29], v[48:49], off offset:512
	s_nop 0
	global_load_dwordx4 v[30:33], v[48:49], off offset:528
	v_lshl_add_u64 v[34:35], v[44:45], 0, v[122:123]
	v_pk_mul_f32 v[24:25], v[42:43], v[24:25] op_sel_hi:[0,1]
	v_pk_mul_f32 v[18:19], v[42:43], v[18:19] op_sel_hi:[0,1]
	v_pk_mul_f32 v[20:21], v[42:43], v[20:21] op_sel_hi:[0,1]
	v_lshl_add_u64 v[34:35], v[34:35], 1, s[28:29]
	s_waitcnt vmcnt(1)
	v_pk_fma_f32 v[24:25], v[114:115], v[24:25], v[28:29]
	v_pk_fma_f32 v[22:23], v[116:117], v[22:23], v[26:27]
	s_waitcnt vmcnt(0)
	v_pk_fma_f32 v[26:27], v[118:119], v[20:21], v[32:33]
	v_pk_fma_f32 v[20:21], v[120:121], v[18:19], v[30:31]
	v_lshl_add_u64 v[28:29], v[150:151], 0, s[16:17]
	v_cvt_pk_bf16_f32 v18, v22, v23
	v_cvt_pk_bf16_f32 v19, v24, v25
	v_cvt_pk_bf16_f32 v20, v20, v21
	v_cvt_pk_bf16_f32 v21, v26, v27
	ds_bpermute_b32 v240, v243, v34
	ds_bpermute_b32 v241, v243, v35
	ds_bpermute_b32 v244, v243, v18
	ds_bpermute_b32 v245, v243, v19
	ds_bpermute_b32 v246, v243, v20
	ds_bpermute_b32 v247, v243, v21
	s_waitcnt lgkmcnt(0)
	global_store_dwordx4 v[240:241], v[244:247], off
	v_lshl_add_u64 v[30:31], v[28:29], 0, v[146:147]
	global_load_dword v26, v[148:149], off offset:704
	v_lshl_add_u64 v[32:33], v[30:31], 2, s[56:57]
	global_load_dwordx4 v[18:21], v[32:33], off
	global_load_dwordx4 v[22:25], v[32:33], off offset:16
	v_lshl_add_u64 v[30:31], v[30:31], 1, s[28:29]
	s_waitcnt vmcnt(2)
	v_pk_mul_f32 v[14:15], v[26:27], v[14:15] op_sel_hi:[0,1]
	v_pk_mul_f32 v[10:11], v[26:27], v[10:11] op_sel_hi:[0,1]
	v_pk_mul_f32 v[12:13], v[26:27], v[12:13] op_sel_hi:[0,1]
	v_pk_mul_f32 v[16:17], v[26:27], v[16:17] op_sel_hi:[0,1]
	s_waitcnt vmcnt(1)
	v_pk_fma_f32 v[14:15], v[126:127], v[14:15], v[18:19]
	s_waitcnt vmcnt(0)
	v_pk_fma_f32 v[18:19], v[128:129], v[12:13], v[24:25]
	v_pk_fma_f32 v[12:13], v[152:153], v[10:11], v[22:23]
	v_pk_fma_f32 v[16:17], v[124:125], v[16:17], v[20:21]
	v_cvt_pk_bf16_f32 v10, v14, v15
	v_pk_mul_f32 v[6:7], v[26:27], v[6:7] op_sel_hi:[0,1]
	v_cvt_pk_bf16_f32 v11, v16, v17
	v_cvt_pk_bf16_f32 v12, v12, v13
	v_cvt_pk_bf16_f32 v13, v18, v19
	ds_bpermute_b32 v240, v243, v30
	ds_bpermute_b32 v241, v243, v31
	ds_bpermute_b32 v244, v243, v10
	ds_bpermute_b32 v245, v243, v11
	ds_bpermute_b32 v246, v243, v12
	ds_bpermute_b32 v247, v243, v13
	s_waitcnt lgkmcnt(0)
	global_store_dwordx4 v[240:241], v[244:247], off
	global_load_dwordx4 v[10:13], v[32:33], off offset:512
	s_nop 0
	global_load_dwordx4 v[14:17], v[32:33], off offset:528
	v_lshl_add_u64 v[18:19], v[28:29], 0, v[122:123]
	v_pk_mul_f32 v[2:3], v[26:27], v[2:3] op_sel_hi:[0,1]
	v_pk_mul_f32 v[4:5], v[26:27], v[4:5] op_sel_hi:[0,1]
	v_lshl_add_u64 v[18:19], v[18:19], 1, s[28:29]
	v_pk_mul_f32 v[8:9], v[26:27], v[8:9] op_sel_hi:[0,1]
	s_waitcnt vmcnt(1)
	v_pk_fma_f32 v[6:7], v[116:117], v[6:7], v[10:11]
	s_waitcnt vmcnt(0)
	v_pk_fma_f32 v[10:11], v[118:119], v[4:5], v[16:17]
	v_pk_fma_f32 v[4:5], v[120:121], v[2:3], v[14:15]
	v_pk_fma_f32 v[8:9], v[114:115], v[8:9], v[12:13]
	v_cvt_pk_bf16_f32 v2, v6, v7
	s_nop 0
	v_cvt_pk_bf16_f32 v3, v8, v9
	v_cvt_pk_bf16_f32 v4, v4, v5
	v_cvt_pk_bf16_f32 v5, v10, v11
	ds_bpermute_b32 v240, v243, v18
	ds_bpermute_b32 v241, v243, v19
	ds_bpermute_b32 v244, v243, v2
	ds_bpermute_b32 v245, v243, v3
	ds_bpermute_b32 v246, v243, v4
	ds_bpermute_b32 v247, v243, v5
	s_waitcnt lgkmcnt(0)
	global_store_dwordx4 v[240:241], v[244:247], off
	s_cbranch_vccnz .LBB0_1224
	s_andn2_b64 vcc, exec, s[4:5]
	s_cbranch_vccnz .LBB0_1223
	s_barrier
	s_branch .LBB0_1223

.LBB0_1395:
	v_mbcnt_lo_u32_b32 v243, -1, 0
	v_mbcnt_hi_u32_b32 v243, -1, v243
	v_lshrrev_b32_e32 v244, 2, v243
	v_and_b32_e32 v243, 3, v243
	v_lshl_add_u32 v243, v243, 4, v244
	v_lshlrev_b32_e32 v243, 2, v243
	v_lshl_add_u32 v162, s0, 8, v164
	v_ashrrev_i32_e32 v163, 31, v162
	v_lshl_add_u64 v[160:161], v[162:163], 2, s[66:67]
	v_lshl_or_b32 v172, s1, 8, v166
	global_load_dword v170, v[160:161], off
	v_ashrrev_i32_e32 v173, 31, v172
	v_lshl_add_u64 v[104:105], v[172:173], 2, s[6:7]
	global_load_dwordx4 v[116:119], v[104:105], off
	global_load_dwordx4 v[112:115], v[104:105], off offset:16
	global_load_dwordx4 v[108:111], v[104:105], off offset:512
	s_nop 0
	global_load_dwordx4 v[104:107], v[104:105], off offset:528
	v_cvt_f32_i32_e32 v143, v143
	v_cvt_f32_i32_e32 v142, v142
	v_cvt_f32_i32_e32 v141, v141
	v_cvt_f32_i32_e32 v140, v140
	v_cvt_f32_i32_e32 v139, v139
	v_cvt_f32_i32_e32 v138, v138
	v_cvt_f32_i32_e32 v137, v137
	v_cvt_f32_i32_e32 v136, v136
	v_cvt_f32_i32_e32 v135, v135
	v_cvt_f32_i32_e32 v134, v134
	v_cvt_f32_i32_e32 v133, v133
	v_cvt_f32_i32_e32 v132, v132
	v_cvt_f32_i32_e32 v177, v131
	v_cvt_f32_i32_e32 v176, v130
	v_cvt_f32_i32_e32 v179, v129
	v_cvt_f32_i32_e32 v178, v128
	v_lshlrev_b64 v[128:129], 12, v[162:163]
	v_or_b32_e32 v180, 16, v162
	v_lshlrev_b64 v[130:131], 1, v[172:173]
	v_lshl_add_u64 v[128:129], s[34:35], 0, v[128:129]
	v_ashrrev_i32_e32 v181, 31, v180
	v_lshl_add_u64 v[128:129], v[128:129], 0, v[130:131]
	v_lshl_add_u64 v[172:173], v[180:181], 2, s[66:67]
	v_cvt_f32_i32_e32 v127, v127
	v_cvt_f32_i32_e32 v126, v126
	v_cvt_f32_i32_e32 v125, v125
	v_cvt_f32_i32_e32 v124, v124
	v_cvt_f32_i32_e32 v123, v123
	v_cvt_f32_i32_e32 v122, v122
	v_cvt_f32_i32_e32 v121, v121
	v_cvt_f32_i32_e32 v120, v120
	v_cvt_f32_i32_e32 v99, v99
	v_cvt_f32_i32_e32 v98, v98
	v_cvt_f32_i32_e32 v97, v97
	v_cvt_f32_i32_e32 v96, v96
	v_cvt_f32_i32_e32 v103, v103
	v_cvt_f32_i32_e32 v102, v102
	v_cvt_f32_i32_e32 v101, v101
	v_cvt_f32_i32_e32 v100, v100
	v_cvt_f32_i32_e32 v95, v95
	v_cvt_f32_i32_e32 v94, v94
	v_cvt_f32_i32_e32 v93, v93
	v_cvt_f32_i32_e32 v92, v92
	v_cvt_f32_i32_e32 v91, v91
	v_cvt_f32_i32_e32 v90, v90
	v_cvt_f32_i32_e32 v89, v89
	v_cvt_f32_i32_e32 v88, v88
	v_cvt_f32_i32_e32 v83, v83
	v_cvt_f32_i32_e32 v82, v82
	v_cvt_f32_i32_e32 v81, v81
	v_cvt_f32_i32_e32 v80, v80
	v_cvt_f32_i32_e32 v87, v87
	v_cvt_f32_i32_e32 v86, v86
	v_cvt_f32_i32_e32 v85, v85
	v_cvt_f32_i32_e32 v84, v84
	v_cvt_f32_i32_e32 v79, v79
	v_cvt_f32_i32_e32 v78, v78
	v_cvt_f32_i32_e32 v77, v77
	v_cvt_f32_i32_e32 v76, v76
	v_cvt_f32_i32_e32 v75, v75
	v_cvt_f32_i32_e32 v74, v74
	v_cvt_f32_i32_e32 v73, v73
	v_cvt_f32_i32_e32 v72, v72
	v_cvt_f32_i32_e32 v67, v67
	v_cvt_f32_i32_e32 v66, v66
	v_cvt_f32_i32_e32 v65, v65
	v_cvt_f32_i32_e32 v64, v64
	v_cvt_f32_i32_e32 v71, v71
	v_cvt_f32_i32_e32 v70, v70
	v_cvt_f32_i32_e32 v69, v69
	v_cvt_f32_i32_e32 v68, v68
	v_cvt_f32_i32_e32 v63, v63
	v_cvt_f32_i32_e32 v62, v62
	v_cvt_f32_i32_e32 v61, v61
	v_cvt_f32_i32_e32 v60, v60
	v_cvt_f32_i32_e32 v59, v59
	s_waitcnt vmcnt(0)
	v_pk_mul_f32 v[140:141], v[170:171], v[140:141] op_sel_hi:[0,1]
	v_pk_mul_f32 v[142:143], v[170:171], v[142:143] op_sel_hi:[0,1]
	v_pk_mul_f32 v[136:137], v[170:171], v[136:137] op_sel_hi:[0,1]
	v_pk_mul_f32 v[138:139], v[170:171], v[138:139] op_sel_hi:[0,1]
	v_pk_mul_f32 v[132:133], v[170:171], v[132:133] op_sel_hi:[0,1]
	v_pk_mul_f32 v[134:135], v[170:171], v[134:135] op_sel_hi:[0,1]
	v_pk_mul_f32 v[178:179], v[170:171], v[178:179] op_sel_hi:[0,1]
	v_pk_mul_f32 v[170:171], v[170:171], v[176:177] op_sel_hi:[0,1]
	v_pk_mul_f32 v[142:143], v[118:119], v[142:143]
	v_pk_mul_f32 v[140:141], v[116:117], v[140:141]
	v_pk_mul_f32 v[138:139], v[114:115], v[138:139]
	v_pk_mul_f32 v[136:137], v[112:113], v[136:137]
	v_pk_mul_f32 v[176:177], v[110:111], v[134:135]
	v_pk_mul_f32 v[182:183], v[108:109], v[132:133]
	v_cvt_pk_bf16_f32 v132, v140, v141
	v_cvt_pk_bf16_f32 v133, v142, v143
	v_cvt_pk_bf16_f32 v134, v136, v137
	v_cvt_pk_bf16_f32 v135, v138, v139
	v_pk_mul_f32 v[170:171], v[106:107], v[170:171]
	v_pk_mul_f32 v[178:179], v[104:105], v[178:179]
	ds_bpermute_b32 v240, v243, v128
	ds_bpermute_b32 v241, v243, v129
	ds_bpermute_b32 v244, v243, v132
	ds_bpermute_b32 v245, v243, v133
	ds_bpermute_b32 v246, v243, v134
	ds_bpermute_b32 v247, v243, v135
	s_waitcnt lgkmcnt(0)
	global_store_dwordx4 v[240:241], v[244:247], off
	v_lshlrev_b64 v[136:137], 12, v[180:181]
	v_lshl_add_u64 v[136:137], s[34:35], 0, v[136:137]
	v_cvt_pk_bf16_f32 v132, v182, v183
	v_cvt_pk_bf16_f32 v133, v176, v177
	v_cvt_pk_bf16_f32 v134, v178, v179
	v_cvt_pk_bf16_f32 v135, v170, v171
	ds_bpermute_b32 v240, v243, v128
	ds_bpermute_b32 v241, v243, v129
	ds_bpermute_b32 v244, v243, v132
	ds_bpermute_b32 v245, v243, v133
	ds_bpermute_b32 v246, v243, v134
	ds_bpermute_b32 v247, v243, v135
	s_waitcnt lgkmcnt(0)
	global_store_dwordx4 v[240:241], v[244:247], off offset:256
	global_load_dword v132, v[172:173], off
	v_lshl_add_u64 v[136:137], v[136:137], 0, v[130:131]
	v_or_b32_e32 v134, 32, v162
	v_ashrrev_i32_e32 v135, 31, v134
	v_lshl_add_u64 v[138:139], v[134:135], 2, s[66:67]
	v_cvt_f32_i32_e32 v58, v58
	v_cvt_f32_i32_e32 v57, v57
	v_cvt_f32_i32_e32 v56, v56
	v_cvt_f32_i32_e32 v51, v51
	v_cvt_f32_i32_e32 v50, v50
	v_cvt_f32_i32_e32 v49, v49
	v_cvt_f32_i32_e32 v48, v48
	v_cvt_f32_i32_e32 v55, v55
	v_cvt_f32_i32_e32 v54, v54
	v_cvt_f32_i32_e32 v53, v53
	v_cvt_f32_i32_e32 v52, v52
	s_mov_b64 s[0:1], 0x80000
	v_cvt_f32_i32_e32 v47, v47
	v_cvt_f32_i32_e32 v46, v46
	v_cvt_f32_i32_e32 v45, v45
	v_cvt_f32_i32_e32 v44, v44
	v_cvt_f32_i32_e32 v43, v43
	v_cvt_f32_i32_e32 v42, v42
	v_cvt_f32_i32_e32 v41, v41
	v_cvt_f32_i32_e32 v40, v40
	v_cvt_f32_i32_e32 v35, v35
	v_cvt_f32_i32_e32 v34, v34
	v_cvt_f32_i32_e32 v33, v33
	v_cvt_f32_i32_e32 v32, v32
	v_cvt_f32_i32_e32 v39, v39
	v_cvt_f32_i32_e32 v38, v38
	v_cvt_f32_i32_e32 v37, v37
	v_cvt_f32_i32_e32 v36, v36
	v_cvt_f32_i32_e32 v31, v31
	v_cvt_f32_i32_e32 v30, v30
	v_cvt_f32_i32_e32 v29, v29
	v_cvt_f32_i32_e32 v28, v28
	v_cvt_f32_i32_e32 v27, v27
	v_cvt_f32_i32_e32 v26, v26
	v_cvt_f32_i32_e32 v25, v25
	v_cvt_f32_i32_e32 v24, v24
	v_cvt_f32_i32_e32 v19, v19
	v_cvt_f32_i32_e32 v18, v18
	v_cvt_f32_i32_e32 v17, v17
	v_cvt_f32_i32_e32 v16, v16
	v_cvt_f32_i32_e32 v23, v23
	v_cvt_f32_i32_e32 v22, v22
	v_cvt_f32_i32_e32 v21, v21
	v_cvt_f32_i32_e32 v20, v20
	v_cvt_f32_i32_e32 v15, v15
	v_cvt_f32_i32_e32 v14, v14
	v_cvt_f32_i32_e32 v13, v13
	v_cvt_f32_i32_e32 v12, v12
	v_cvt_f32_i32_e32 v11, v11
	v_cvt_f32_i32_e32 v10, v10
	v_cvt_f32_i32_e32 v9, v9
	v_cvt_f32_i32_e32 v8, v8
	v_cvt_f32_i32_e32 v3, v3
	v_cvt_f32_i32_e32 v2, v2
	v_cvt_f32_i32_e32 v1, v1
	v_cvt_f32_i32_e32 v0, v0
	v_cvt_f32_i32_e32 v7, v7
	v_cvt_f32_i32_e32 v6, v6
	v_cvt_f32_i32_e32 v5, v5
	v_cvt_f32_i32_e32 v4, v4
	s_mov_b32 s76, s80
	s_waitcnt vmcnt(0)
	v_pk_mul_f32 v[124:125], v[132:133], v[124:125] op_sel_hi:[0,1]
	v_pk_mul_f32 v[126:127], v[132:133], v[126:127] op_sel_hi:[0,1]
	v_pk_mul_f32 v[120:121], v[132:133], v[120:121] op_sel_hi:[0,1]
	v_pk_mul_f32 v[122:123], v[132:133], v[122:123] op_sel_hi:[0,1]
	v_pk_mul_f32 v[96:97], v[132:133], v[96:97] op_sel_hi:[0,1]
	v_pk_mul_f32 v[98:99], v[132:133], v[98:99] op_sel_hi:[0,1]
	v_pk_mul_f32 v[100:101], v[132:133], v[100:101] op_sel_hi:[0,1]
	v_pk_mul_f32 v[102:103], v[132:133], v[102:103] op_sel_hi:[0,1]
	v_pk_mul_f32 v[126:127], v[118:119], v[126:127]
	v_pk_mul_f32 v[124:125], v[116:117], v[124:125]
	v_pk_mul_f32 v[122:123], v[114:115], v[122:123]
	v_pk_mul_f32 v[120:121], v[112:113], v[120:121]
	v_pk_mul_f32 v[132:133], v[106:107], v[98:99]
	v_pk_mul_f32 v[140:141], v[104:105], v[96:97]
	v_cvt_pk_bf16_f32 v96, v124, v125
	v_cvt_pk_bf16_f32 v97, v126, v127
	v_cvt_pk_bf16_f32 v98, v120, v121
	v_cvt_pk_bf16_f32 v99, v122, v123
	v_pk_mul_f32 v[102:103], v[110:111], v[102:103]
	v_pk_mul_f32 v[100:101], v[108:109], v[100:101]
	ds_bpermute_b32 v240, v243, v136
	ds_bpermute_b32 v241, v243, v137
	ds_bpermute_b32 v244, v243, v96
	ds_bpermute_b32 v245, v243, v97
	ds_bpermute_b32 v246, v243, v98
	ds_bpermute_b32 v247, v243, v99
	s_waitcnt lgkmcnt(0)
	global_store_dwordx4 v[240:241], v[244:247], off
	s_nop 1
	v_cvt_pk_bf16_f32 v96, v100, v101
	v_cvt_pk_bf16_f32 v97, v102, v103
	v_cvt_pk_bf16_f32 v98, v140, v141
	v_cvt_pk_bf16_f32 v99, v132, v133
	ds_bpermute_b32 v240, v243, v136
	ds_bpermute_b32 v241, v243, v137
	ds_bpermute_b32 v244, v243, v96
	ds_bpermute_b32 v245, v243, v97
	ds_bpermute_b32 v246, v243, v98
	ds_bpermute_b32 v247, v243, v99
	s_waitcnt lgkmcnt(0)
	global_store_dwordx4 v[240:241], v[244:247], off offset:256
	global_load_dword v96, v[138:139], off
	v_lshlrev_b64 v[100:101], 12, v[134:135]
	v_or_b32_e32 v98, 48, v162
	v_lshl_add_u64 v[100:101], s[34:35], 0, v[100:101]
	v_ashrrev_i32_e32 v99, 31, v98
	v_lshl_add_u64 v[100:101], v[100:101], 0, v[130:131]
	v_lshl_add_u64 v[102:103], v[98:99], 2, s[66:67]
	s_waitcnt vmcnt(0)
	v_pk_mul_f32 v[92:93], v[96:97], v[92:93] op_sel_hi:[0,1]
	v_pk_mul_f32 v[94:95], v[96:97], v[94:95] op_sel_hi:[0,1]
	v_pk_mul_f32 v[88:89], v[96:97], v[88:89] op_sel_hi:[0,1]
	v_pk_mul_f32 v[90:91], v[96:97], v[90:91] op_sel_hi:[0,1]
	v_pk_mul_f32 v[80:81], v[96:97], v[80:81] op_sel_hi:[0,1]
	v_pk_mul_f32 v[82:83], v[96:97], v[82:83] op_sel_hi:[0,1]
	v_pk_mul_f32 v[84:85], v[96:97], v[84:85] op_sel_hi:[0,1]
	v_pk_mul_f32 v[86:87], v[96:97], v[86:87] op_sel_hi:[0,1]
	v_pk_mul_f32 v[94:95], v[118:119], v[94:95]
	v_pk_mul_f32 v[92:93], v[116:117], v[92:93]
	v_pk_mul_f32 v[90:91], v[114:115], v[90:91]
	v_pk_mul_f32 v[88:89], v[112:113], v[88:89]
	v_pk_mul_f32 v[96:97], v[106:107], v[82:83]
	v_pk_mul_f32 v[120:121], v[104:105], v[80:81]
	v_cvt_pk_bf16_f32 v80, v92, v93
	v_cvt_pk_bf16_f32 v81, v94, v95
	v_cvt_pk_bf16_f32 v82, v88, v89
	v_cvt_pk_bf16_f32 v83, v90, v91
	v_pk_mul_f32 v[86:87], v[110:111], v[86:87]
	v_pk_mul_f32 v[84:85], v[108:109], v[84:85]
	ds_bpermute_b32 v240, v243, v100
	ds_bpermute_b32 v241, v243, v101
	ds_bpermute_b32 v244, v243, v80
	ds_bpermute_b32 v245, v243, v81
	ds_bpermute_b32 v246, v243, v82
	ds_bpermute_b32 v247, v243, v83
	s_waitcnt lgkmcnt(0)
	global_store_dwordx4 v[240:241], v[244:247], off
	s_nop 1
	v_cvt_pk_bf16_f32 v80, v84, v85
	v_cvt_pk_bf16_f32 v81, v86, v87
	v_cvt_pk_bf16_f32 v82, v120, v121
	v_cvt_pk_bf16_f32 v83, v96, v97
	ds_bpermute_b32 v240, v243, v100
	ds_bpermute_b32 v241, v243, v101
	ds_bpermute_b32 v244, v243, v80
	ds_bpermute_b32 v245, v243, v81
	ds_bpermute_b32 v246, v243, v82
	ds_bpermute_b32 v247, v243, v83
	s_waitcnt lgkmcnt(0)
	global_store_dwordx4 v[240:241], v[244:247], off offset:256
	global_load_dword v80, v[102:103], off
	s_waitcnt vmcnt(0)
	v_pk_mul_f32 v[76:77], v[80:81], v[76:77] op_sel_hi:[0,1]
	v_lshlrev_b64 v[82:83], 12, v[98:99]
	v_lshl_add_u64 v[82:83], s[34:35], 0, v[82:83]
	v_pk_mul_f32 v[78:79], v[80:81], v[78:79] op_sel_hi:[0,1]
	v_pk_mul_f32 v[72:73], v[80:81], v[72:73] op_sel_hi:[0,1]
	v_pk_mul_f32 v[74:75], v[80:81], v[74:75] op_sel_hi:[0,1]
	v_pk_mul_f32 v[64:65], v[80:81], v[64:65] op_sel_hi:[0,1]
	v_pk_mul_f32 v[66:67], v[80:81], v[66:67] op_sel_hi:[0,1]
	v_lshl_add_u64 v[82:83], v[82:83], 0, v[130:131]
	v_pk_mul_f32 v[68:69], v[80:81], v[68:69] op_sel_hi:[0,1]
	v_pk_mul_f32 v[70:71], v[80:81], v[70:71] op_sel_hi:[0,1]
	v_pk_mul_f32 v[78:79], v[118:119], v[78:79]
	v_pk_mul_f32 v[76:77], v[116:117], v[76:77]
	v_pk_mul_f32 v[74:75], v[114:115], v[74:75]
	v_pk_mul_f32 v[72:73], v[112:113], v[72:73]
	v_pk_mul_f32 v[80:81], v[106:107], v[66:67]
	v_pk_mul_f32 v[84:85], v[104:105], v[64:65]
	v_cvt_pk_bf16_f32 v64, v76, v77
	v_cvt_pk_bf16_f32 v65, v78, v79
	v_cvt_pk_bf16_f32 v66, v72, v73
	v_cvt_pk_bf16_f32 v67, v74, v75
	v_pk_mul_f32 v[70:71], v[110:111], v[70:71]
	v_pk_mul_f32 v[68:69], v[108:109], v[68:69]
	ds_bpermute_b32 v240, v243, v82
	ds_bpermute_b32 v241, v243, v83
	ds_bpermute_b32 v244, v243, v64
	ds_bpermute_b32 v245, v243, v65
	ds_bpermute_b32 v246, v243, v66
	ds_bpermute_b32 v247, v243, v67
	s_waitcnt lgkmcnt(0)
	global_store_dwordx4 v[240:241], v[244:247], off
	s_nop 1
	v_cvt_pk_bf16_f32 v64, v68, v69
	v_cvt_pk_bf16_f32 v65, v70, v71
	v_cvt_pk_bf16_f32 v66, v84, v85
	v_cvt_pk_bf16_f32 v67, v80, v81
	ds_bpermute_b32 v240, v243, v82
	ds_bpermute_b32 v241, v243, v83
	ds_bpermute_b32 v244, v243, v64
	ds_bpermute_b32 v245, v243, v65
	ds_bpermute_b32 v246, v243, v66
	ds_bpermute_b32 v247, v243, v67
	s_waitcnt lgkmcnt(0)
	global_store_dwordx4 v[240:241], v[244:247], off offset:256
	global_load_dword v64, v[160:161], off offset:512
	v_add_co_u32_e32 v68, vcc, s65, v128
	v_lshl_add_u64 v[66:67], v[128:129], 0, s[0:1]
	s_nop 0
	v_addc_co_u32_e32 v69, vcc, 0, v129, vcc
	s_waitcnt vmcnt(0)
	v_pk_mul_f32 v[60:61], v[64:65], v[60:61] op_sel_hi:[0,1]
	v_pk_mul_f32 v[62:63], v[64:65], v[62:63] op_sel_hi:[0,1]
	v_pk_mul_f32 v[56:57], v[64:65], v[56:57] op_sel_hi:[0,1]
	v_pk_mul_f32 v[58:59], v[64:65], v[58:59] op_sel_hi:[0,1]
	v_pk_mul_f32 v[48:49], v[64:65], v[48:49] op_sel_hi:[0,1]
	v_pk_mul_f32 v[50:51], v[64:65], v[50:51] op_sel_hi:[0,1]
	v_pk_mul_f32 v[52:53], v[64:65], v[52:53] op_sel_hi:[0,1]
	v_pk_mul_f32 v[54:55], v[64:65], v[54:55] op_sel_hi:[0,1]
	v_pk_mul_f32 v[62:63], v[118:119], v[62:63]
	v_pk_mul_f32 v[60:61], v[116:117], v[60:61]
	v_pk_mul_f32 v[58:59], v[114:115], v[58:59]
	v_pk_mul_f32 v[56:57], v[112:113], v[56:57]
	v_pk_mul_f32 v[64:65], v[106:107], v[50:51]
	v_pk_mul_f32 v[70:71], v[104:105], v[48:49]
	v_cvt_pk_bf16_f32 v48, v60, v61
	v_cvt_pk_bf16_f32 v49, v62, v63
	v_cvt_pk_bf16_f32 v50, v56, v57
	v_cvt_pk_bf16_f32 v51, v58, v59
	v_pk_mul_f32 v[54:55], v[110:111], v[54:55]
	v_pk_mul_f32 v[52:53], v[108:109], v[52:53]
	ds_bpermute_b32 v240, v243, v68
	ds_bpermute_b32 v241, v243, v69
	ds_bpermute_b32 v244, v243, v48
	ds_bpermute_b32 v245, v243, v49
	ds_bpermute_b32 v246, v243, v50
	ds_bpermute_b32 v247, v243, v51
	s_waitcnt lgkmcnt(0)
	global_store_dwordx4 v[240:241], v[244:247], off
	s_nop 1
	v_cvt_pk_bf16_f32 v48, v52, v53
	v_cvt_pk_bf16_f32 v49, v54, v55
	v_cvt_pk_bf16_f32 v50, v70, v71
	v_cvt_pk_bf16_f32 v51, v64, v65
	ds_bpermute_b32 v240, v243, v66
	ds_bpermute_b32 v241, v243, v67
	ds_bpermute_b32 v244, v243, v48
	ds_bpermute_b32 v245, v243, v49
	ds_bpermute_b32 v246, v243, v50
	ds_bpermute_b32 v247, v243, v51
	s_waitcnt lgkmcnt(0)
	global_store_dwordx4 v[240:241], v[244:247], off offset:256
	global_load_dword v48, v[160:161], off offset:576
	v_add_co_u32_e32 v52, vcc, s68, v128
	v_lshl_add_u64 v[50:51], v[128:129], 0, s[12:13]
	s_nop 0
	v_addc_co_u32_e32 v53, vcc, 0, v129, vcc
	s_waitcnt vmcnt(0)
	v_pk_mul_f32 v[44:45], v[48:49], v[44:45] op_sel_hi:[0,1]
	v_pk_mul_f32 v[46:47], v[48:49], v[46:47] op_sel_hi:[0,1]
	v_pk_mul_f32 v[40:41], v[48:49], v[40:41] op_sel_hi:[0,1]
	v_pk_mul_f32 v[42:43], v[48:49], v[42:43] op_sel_hi:[0,1]
	v_pk_mul_f32 v[32:33], v[48:49], v[32:33] op_sel_hi:[0,1]
	v_pk_mul_f32 v[34:35], v[48:49], v[34:35] op_sel_hi:[0,1]
	v_pk_mul_f32 v[36:37], v[48:49], v[36:37] op_sel_hi:[0,1]
	v_pk_mul_f32 v[38:39], v[48:49], v[38:39] op_sel_hi:[0,1]
	v_pk_mul_f32 v[46:47], v[118:119], v[46:47]
	v_pk_mul_f32 v[44:45], v[116:117], v[44:45]
	v_pk_mul_f32 v[42:43], v[114:115], v[42:43]
	v_pk_mul_f32 v[40:41], v[112:113], v[40:41]
	v_pk_mul_f32 v[48:49], v[106:107], v[34:35]
	v_pk_mul_f32 v[54:55], v[104:105], v[32:33]
	v_cvt_pk_bf16_f32 v32, v44, v45
	v_cvt_pk_bf16_f32 v33, v46, v47
	v_cvt_pk_bf16_f32 v34, v40, v41
	v_cvt_pk_bf16_f32 v35, v42, v43
	v_pk_mul_f32 v[38:39], v[110:111], v[38:39]
	v_pk_mul_f32 v[36:37], v[108:109], v[36:37]
	ds_bpermute_b32 v240, v243, v52
	ds_bpermute_b32 v241, v243, v53
	ds_bpermute_b32 v244, v243, v32
	ds_bpermute_b32 v245, v243, v33
	ds_bpermute_b32 v246, v243, v34
	ds_bpermute_b32 v247, v243, v35
	s_waitcnt lgkmcnt(0)
	global_store_dwordx4 v[240:241], v[244:247], off
	s_nop 1
	v_cvt_pk_bf16_f32 v32, v36, v37
	v_cvt_pk_bf16_f32 v33, v38, v39
	v_cvt_pk_bf16_f32 v34, v54, v55
	v_cvt_pk_bf16_f32 v35, v48, v49
	ds_bpermute_b32 v240, v243, v50
	ds_bpermute_b32 v241, v243, v51
	ds_bpermute_b32 v244, v243, v32
	ds_bpermute_b32 v245, v243, v33
	ds_bpermute_b32 v246, v243, v34
	ds_bpermute_b32 v247, v243, v35
	s_waitcnt lgkmcnt(0)
	global_store_dwordx4 v[240:241], v[244:247], off offset:256
	global_load_dword v32, v[160:161], off offset:640
	v_add_co_u32_e32 v36, vcc, s69, v128
	v_lshl_add_u64 v[34:35], v[128:129], 0, s[14:15]
	s_nop 0
	v_addc_co_u32_e32 v37, vcc, 0, v129, vcc
	s_andn2_b64 vcc, exec, s[2:3]
	s_waitcnt vmcnt(0)
	v_pk_mul_f32 v[28:29], v[32:33], v[28:29] op_sel_hi:[0,1]
	v_pk_mul_f32 v[30:31], v[32:33], v[30:31] op_sel_hi:[0,1]
	v_pk_mul_f32 v[24:25], v[32:33], v[24:25] op_sel_hi:[0,1]
	v_pk_mul_f32 v[26:27], v[32:33], v[26:27] op_sel_hi:[0,1]
	v_pk_mul_f32 v[16:17], v[32:33], v[16:17] op_sel_hi:[0,1]
	v_pk_mul_f32 v[18:19], v[32:33], v[18:19] op_sel_hi:[0,1]
	v_pk_mul_f32 v[20:21], v[32:33], v[20:21] op_sel_hi:[0,1]
	v_pk_mul_f32 v[22:23], v[32:33], v[22:23] op_sel_hi:[0,1]
	v_pk_mul_f32 v[30:31], v[118:119], v[30:31]
	v_pk_mul_f32 v[28:29], v[116:117], v[28:29]
	v_pk_mul_f32 v[26:27], v[114:115], v[26:27]
	v_pk_mul_f32 v[24:25], v[112:113], v[24:25]
	v_pk_mul_f32 v[32:33], v[106:107], v[18:19]
	v_pk_mul_f32 v[38:39], v[104:105], v[16:17]
	v_cvt_pk_bf16_f32 v16, v28, v29
	v_cvt_pk_bf16_f32 v17, v30, v31
	v_cvt_pk_bf16_f32 v18, v24, v25
	v_cvt_pk_bf16_f32 v19, v26, v27
	v_pk_mul_f32 v[22:23], v[110:111], v[22:23]
	v_pk_mul_f32 v[20:21], v[108:109], v[20:21]
	ds_bpermute_b32 v240, v243, v36
	ds_bpermute_b32 v241, v243, v37
	ds_bpermute_b32 v244, v243, v16
	ds_bpermute_b32 v245, v243, v17
	ds_bpermute_b32 v246, v243, v18
	ds_bpermute_b32 v247, v243, v19
	s_waitcnt lgkmcnt(0)
	global_store_dwordx4 v[240:241], v[244:247], off
	s_nop 1
	v_cvt_pk_bf16_f32 v16, v20, v21
	v_cvt_pk_bf16_f32 v17, v22, v23
	v_cvt_pk_bf16_f32 v18, v38, v39
	v_cvt_pk_bf16_f32 v19, v32, v33
	ds_bpermute_b32 v240, v243, v34
	ds_bpermute_b32 v241, v243, v35
	ds_bpermute_b32 v244, v243, v16
	ds_bpermute_b32 v245, v243, v17
	ds_bpermute_b32 v246, v243, v18
	ds_bpermute_b32 v247, v243, v19
	s_waitcnt lgkmcnt(0)
	global_store_dwordx4 v[240:241], v[244:247], off offset:256
	global_load_dword v16, v[160:161], off offset:704
	v_add_co_u32_e64 v20, s[0:1], s70, v128
	v_lshl_add_u64 v[18:19], v[128:129], 0, s[16:17]
	s_nop 0
	v_addc_co_u32_e64 v21, s[0:1], 0, v129, s[0:1]
	s_mov_b64 s[0:1], -1
	s_waitcnt vmcnt(0)
	v_pk_mul_f32 v[12:13], v[16:17], v[12:13] op_sel_hi:[0,1]
	v_pk_mul_f32 v[14:15], v[16:17], v[14:15] op_sel_hi:[0,1]
	v_pk_mul_f32 v[8:9], v[16:17], v[8:9] op_sel_hi:[0,1]
	v_pk_mul_f32 v[10:11], v[16:17], v[10:11] op_sel_hi:[0,1]
	v_pk_mul_f32 v[0:1], v[16:17], v[0:1] op_sel_hi:[0,1]
	v_pk_mul_f32 v[2:3], v[16:17], v[2:3] op_sel_hi:[0,1]
	v_pk_mul_f32 v[4:5], v[16:17], v[4:5] op_sel_hi:[0,1]
	v_pk_mul_f32 v[6:7], v[16:17], v[6:7] op_sel_hi:[0,1]
	v_pk_mul_f32 v[14:15], v[118:119], v[14:15]
	v_pk_mul_f32 v[12:13], v[116:117], v[12:13]
	v_pk_mul_f32 v[10:11], v[114:115], v[10:11]
	v_pk_mul_f32 v[8:9], v[112:113], v[8:9]
	v_pk_mul_f32 v[16:17], v[106:107], v[2:3]
	v_pk_mul_f32 v[22:23], v[104:105], v[0:1]
	v_cvt_pk_bf16_f32 v0, v12, v13
	v_cvt_pk_bf16_f32 v1, v14, v15
	v_cvt_pk_bf16_f32 v2, v8, v9
	v_cvt_pk_bf16_f32 v3, v10, v11
	v_pk_mul_f32 v[6:7], v[110:111], v[6:7]
	v_pk_mul_f32 v[4:5], v[108:109], v[4:5]
	ds_bpermute_b32 v240, v243, v20
	ds_bpermute_b32 v241, v243, v21
	ds_bpermute_b32 v244, v243, v0
	ds_bpermute_b32 v245, v243, v1
	ds_bpermute_b32 v246, v243, v2
	ds_bpermute_b32 v247, v243, v3
	s_waitcnt lgkmcnt(0)
	global_store_dwordx4 v[240:241], v[244:247], off
	s_nop 1
	v_cvt_pk_bf16_f32 v0, v4, v5
	v_cvt_pk_bf16_f32 v1, v6, v7
	v_cvt_pk_bf16_f32 v2, v22, v23
	v_cvt_pk_bf16_f32 v3, v16, v17
	ds_bpermute_b32 v240, v243, v18
	ds_bpermute_b32 v241, v243, v19
	ds_bpermute_b32 v244, v243, v0
	ds_bpermute_b32 v245, v243, v1
	ds_bpermute_b32 v246, v243, v2
	ds_bpermute_b32 v247, v243, v3
	s_waitcnt lgkmcnt(0)
	global_store_dwordx4 v[240:241], v[244:247], off offset:256
	s_cbranch_vccnz .LBB0_1384
	s_andn2_b64 vcc, exec, s[4:5]
	s_cbranch_vccnz .LBB0_1383
	s_barrier
	s_branch .LBB0_1383
